# gate/up and down epilogues: 96 dead zero-initialisations of v_cvt_pk_fp8_f32 destinations removed (both halves are written by the two converts before any read)
# baseline (speedup 1.0000x reference)
.LBB0_1546:
	s_mov_b32 s73, 0xc2700000
	v_mov_b32_e32 v184, 0x41898193
	v_lshlrev_b32_e32 v150, 16, v86
	v_and_b32_e32 v151, 0xffff0000, v86
	v_mul_f32_e32 v158, 0x3d800000, v177
	v_pk_fma_f32 v[130:131], v[158:159], v[130:131], v[150:151] op_sel_hi:[0,1,1]
	v_med3_f32 v130, v130, s73, v184
	v_med3_f32 v131, v131, s73, v184
	v_exp_f32_e64 v178, -v130
	v_exp_f32_e64 v179, -v131
	v_lshlrev_b32_e32 v156, 16, v87
	v_and_b32_e32 v157, 0xffff0000, v87
	v_lshlrev_b32_e32 v152, 16, v82
	v_pk_add_f32 v[178:179], v[178:179], 1.0 op_sel_hi:[1,0]
	v_and_b32_e32 v153, 0xffff0000, v82
	v_lshlrev_b32_e32 v154, 16, v83
	v_and_b32_e32 v155, 0xffff0000, v83
	v_pk_fma_f32 v[132:133], v[158:159], v[132:133], v[156:157] op_sel_hi:[0,1,1]
	v_pk_fma_f32 v[134:135], v[158:159], v[134:135], v[152:153] op_sel_hi:[0,1,1]
	v_pk_fma_f32 v[136:137], v[158:159], v[136:137], v[154:155] op_sel_hi:[0,1,1]
	v_med3_f32 v134, v134, s70, v167
	v_med3_f32 v135, v135, s70, v167
	v_med3_f32 v132, v132, s73, v184
	v_med3_f32 v133, v133, s73, v184
	v_pk_mul_f32 v[130:131], v[130:131], v[134:135]
	v_med3_f32 v134, v136, s70, v167
	v_med3_f32 v135, v137, s70, v167
	v_exp_f32_e64 v136, -v132
	v_exp_f32_e64 v137, -v133
	v_lshlrev_b32_e32 v86, 16, v88
	v_and_b32_e32 v87, 0xffff0000, v88
	v_pk_fma_f32 v[122:123], v[158:159], v[122:123], v[86:87] op_sel_hi:[0,1,1]
	v_pk_add_f32 v[136:137], v[136:137], 1.0 op_sel_hi:[1,0]
	v_med3_f32 v122, v122, s73, v184
	v_pk_mul_f32 v[180:181], v[178:179], v[136:137]
	v_rcp_f32_e32 v180, v180
	v_rcp_f32_e32 v181, v181
	s_nop 0
	v_pk_mul_f32 v[182:183], v[180:181], v[136:137]
	v_pk_mul_f32 v[136:137], v[180:181], v[178:179]
	v_pk_mul_f32 v[130:131], v[130:131], v[182:183]
	v_med3_f32 v123, v123, s73, v184
	v_lshlrev_b32_e32 v88, 16, v89
	v_and_b32_e32 v89, 0xffff0000, v89
	v_pk_mul_f32 v[132:133], v[132:133], v[136:137]
	v_lshlrev_b32_e32 v82, 16, v84
	v_pk_mul_f32 v[132:133], v[132:133], v[134:135]
	v_exp_f32_e64 v134, -v122
	v_exp_f32_e64 v135, -v123
	v_and_b32_e32 v83, 0xffff0000, v84
	v_lshlrev_b32_e32 v84, 16, v85
	v_and_b32_e32 v85, 0xffff0000, v85
	v_pk_add_f32 v[134:135], v[134:135], 1.0 op_sel_hi:[1,0]
	v_pk_fma_f32 v[124:125], v[158:159], v[124:125], v[88:89] op_sel_hi:[0,1,1]
	v_pk_fma_f32 v[126:127], v[158:159], v[126:127], v[82:83] op_sel_hi:[0,1,1]
	v_pk_fma_f32 v[128:129], v[158:159], v[128:129], v[84:85] op_sel_hi:[0,1,1]
	v_med3_f32 v126, v126, s70, v167
	v_med3_f32 v127, v127, s70, v167
	v_med3_f32 v124, v124, s73, v184
	v_med3_f32 v125, v125, s73, v184
	v_pk_mul_f32 v[122:123], v[122:123], v[126:127]
	v_med3_f32 v126, v128, s70, v167
	v_med3_f32 v127, v129, s70, v167
	v_exp_f32_e64 v128, -v124
	v_exp_f32_e64 v129, -v125
	v_mov_b32_e32 v142, v0
	s_and_b64 vcc, exec, s[6:7]
	v_pk_add_f32 v[128:129], v[128:129], 1.0 op_sel_hi:[1,0]
	v_readfirstlane_b32 s69, v142
	v_pk_mul_f32 v[180:181], v[134:135], v[128:129]
	v_rcp_f32_e32 v180, v180
	v_rcp_f32_e32 v181, v181
	s_nop 0
	v_pk_mul_f32 v[182:183], v[180:181], v[128:129]
	v_pk_mul_f32 v[128:129], v[180:181], v[134:135]
	v_pk_mul_f32 v[122:123], v[122:123], v[182:183]
	s_ashr_i32 s8, s69, 6
	s_mul_i32 s9, s8, 0xb00
	s_add_i32 s71, s9, 0
	v_pk_mul_f32 v[124:125], v[124:125], v[128:129]
	v_and_b32_e32 v147, 15, v142
	v_pk_mul_f32 v[124:125], v[124:125], v[126:127]
	v_cvt_pk_fp8_f32 v126, v130, v131
	v_cvt_pk_fp8_f32 v127, v122, v123
	v_lshrrev_b32_e32 v123, 1, v142
	s_add_i32 s71, s71, 0x20000
	v_cvt_pk_fp8_f32 v126, v132, v133 op_sel:[0,0,1]
	v_cvt_pk_fp8_f32 v127, v124, v125 op_sel:[0,0,1]
	v_mul_f32_e32 v124, 0x3d800000, v176
	v_mul_u32_u24_e32 v122, 48, v147
	v_and_b32_e32 v123, 24, v123
	v_pk_fma_f32 v[114:115], v[124:125], v[114:115], v[150:151] op_sel_hi:[0,1,1]
	v_add3_u32 v122, s71, v122, v123
	v_med3_f32 v114, v114, s73, v184
	v_med3_f32 v115, v115, s73, v184
	ds_write_b64 v122, v[126:127]
	v_exp_f32_e64 v126, -v114
	v_exp_f32_e64 v127, -v115
	v_pk_fma_f32 v[116:117], v[124:125], v[116:117], v[156:157] op_sel_hi:[0,1,1]
	v_pk_fma_f32 v[118:119], v[124:125], v[118:119], v[152:153] op_sel_hi:[0,1,1]
	v_pk_fma_f32 v[120:121], v[124:125], v[120:121], v[154:155] op_sel_hi:[0,1,1]
	v_pk_add_f32 v[126:127], v[126:127], 1.0 op_sel_hi:[1,0]
	v_med3_f32 v118, v118, s70, v167
	v_med3_f32 v119, v119, s70, v167
	v_med3_f32 v116, v116, s73, v184
	v_med3_f32 v117, v117, s73, v184
	v_pk_fma_f32 v[106:107], v[124:125], v[106:107], v[86:87] op_sel_hi:[0,1,1]
	v_pk_mul_f32 v[114:115], v[114:115], v[118:119]
	v_med3_f32 v118, v120, s70, v167
	v_med3_f32 v119, v121, s70, v167
	v_exp_f32_e64 v120, -v116
	v_exp_f32_e64 v121, -v117
	v_med3_f32 v106, v106, s73, v184
	v_med3_f32 v107, v107, s73, v184
	v_pk_fma_f32 v[108:109], v[124:125], v[108:109], v[88:89] op_sel_hi:[0,1,1]
	v_pk_add_f32 v[120:121], v[120:121], 1.0 op_sel_hi:[1,0]
	v_pk_fma_f32 v[110:111], v[124:125], v[110:111], v[82:83] op_sel_hi:[0,1,1]
	v_pk_mul_f32 v[180:181], v[126:127], v[120:121]
	v_rcp_f32_e32 v180, v180
	v_rcp_f32_e32 v181, v181
	s_nop 0
	v_pk_mul_f32 v[182:183], v[180:181], v[120:121]
	v_pk_mul_f32 v[120:121], v[180:181], v[126:127]
	v_pk_mul_f32 v[114:115], v[114:115], v[182:183]
	v_pk_fma_f32 v[112:113], v[124:125], v[112:113], v[84:85] op_sel_hi:[0,1,1]
	v_med3_f32 v110, v110, s70, v167
	v_med3_f32 v111, v111, s70, v167
	v_pk_mul_f32 v[116:117], v[116:117], v[120:121]
	v_med3_f32 v108, v108, s73, v184
	v_pk_mul_f32 v[116:117], v[116:117], v[118:119]
	v_exp_f32_e64 v118, -v106
	v_exp_f32_e64 v119, -v107
	v_med3_f32 v109, v109, s73, v184
	s_ashr_i32 s69, s69, 2
	s_andn2_b32 s69, s69, 63
	v_pk_add_f32 v[118:119], v[118:119], 1.0 op_sel_hi:[1,0]
	s_lshl_b32 s8, s8, 5
	s_lshl_b32 s9, s80, 7
	s_and_b32 s8, s8, 0x60
	s_or_b32 s8, s8, s9
	s_ashr_i32 s9, s8, 31
	v_pk_mul_f32 v[106:107], v[106:107], v[110:111]
	v_med3_f32 v110, v112, s70, v167
	v_med3_f32 v111, v113, s70, v167
	v_exp_f32_e64 v112, -v108
	v_exp_f32_e64 v113, -v109
	s_nop 0
	v_pk_add_f32 v[112:113], v[112:113], 1.0 op_sel_hi:[1,0]
	s_nop 0
	v_pk_mul_f32 v[180:181], v[118:119], v[112:113]
	v_rcp_f32_e32 v180, v180
	v_rcp_f32_e32 v181, v181
	s_nop 0
	v_pk_mul_f32 v[182:183], v[180:181], v[112:113]
	v_pk_mul_f32 v[112:113], v[180:181], v[118:119]
	v_pk_mul_f32 v[106:107], v[106:107], v[182:183]
	s_nop 0
	v_pk_mul_f32 v[108:109], v[108:109], v[112:113]
	s_nop 0
	v_pk_mul_f32 v[108:109], v[108:109], v[110:111]
	v_cvt_pk_fp8_f32 v110, v114, v115
	v_cvt_pk_fp8_f32 v111, v106, v107
	v_bfe_u32 v106, v142, 1, 5
	v_mul_u32_u24_e32 v107, 48, v106
	v_cvt_pk_fp8_f32 v110, v116, v117 op_sel:[0,0,1]
	v_cvt_pk_fp8_f32 v111, v108, v109 op_sel:[0,0,1]
	v_lshlrev_b32_e32 v108, 4, v142
	v_and_b32_e32 v142, 16, v108
	v_lshl_or_b32 v106, s78, 8, v106
	ds_write_b64 v122, v[110:111] offset:768
	v_add3_u32 v108, s71, v107, v142
	v_add_u32_e32 v106, s69, v106
	ds_read_b128 v[110:113], v108
	v_ashrrev_i32_e32 v107, 31, v106
	v_lshl_add_u32 v114, v106, 10, v142
	s_add_u32 s86, s16, s8
	s_addc_u32 s87, s17, s9
	s_waitcnt lgkmcnt(0)
	global_store_dwordx4 v114, v[110:113], s[86:87]
	s_nop 1
	v_mul_f32_e32 v110, 0x3d800000, v175
	v_pk_fma_f32 v[98:99], v[110:111], v[98:99], v[150:151] op_sel_hi:[0,1,1]
	v_med3_f32 v98, v98, s73, v184
	v_med3_f32 v99, v99, s73, v184
	v_exp_f32_e64 v112, -v98
	v_exp_f32_e64 v113, -v99
	v_pk_fma_f32 v[100:101], v[110:111], v[100:101], v[156:157] op_sel_hi:[0,1,1]
	v_pk_fma_f32 v[102:103], v[110:111], v[102:103], v[152:153] op_sel_hi:[0,1,1]
	v_pk_fma_f32 v[104:105], v[110:111], v[104:105], v[154:155] op_sel_hi:[0,1,1]
	v_pk_add_f32 v[112:113], v[112:113], 1.0 op_sel_hi:[1,0]
	v_med3_f32 v102, v102, s70, v167
	v_med3_f32 v103, v103, s70, v167
	v_med3_f32 v100, v100, s73, v184
	v_med3_f32 v101, v101, s73, v184
	v_pk_fma_f32 v[90:91], v[110:111], v[90:91], v[86:87] op_sel_hi:[0,1,1]
	v_pk_mul_f32 v[98:99], v[98:99], v[102:103]
	v_med3_f32 v102, v104, s70, v167
	v_med3_f32 v103, v105, s70, v167
	v_exp_f32_e64 v104, -v100
	v_exp_f32_e64 v105, -v101
	v_med3_f32 v90, v90, s73, v184
	v_med3_f32 v91, v91, s73, v184
	v_pk_fma_f32 v[92:93], v[110:111], v[92:93], v[88:89] op_sel_hi:[0,1,1]
	v_pk_add_f32 v[104:105], v[104:105], 1.0 op_sel_hi:[1,0]
	v_pk_fma_f32 v[94:95], v[110:111], v[94:95], v[82:83] op_sel_hi:[0,1,1]
	v_pk_mul_f32 v[180:181], v[112:113], v[104:105]
	v_rcp_f32_e32 v180, v180
	v_rcp_f32_e32 v181, v181
	s_nop 0
	v_pk_mul_f32 v[182:183], v[180:181], v[104:105]
	v_pk_mul_f32 v[104:105], v[180:181], v[112:113]
	v_pk_mul_f32 v[98:99], v[98:99], v[182:183]
	v_pk_fma_f32 v[96:97], v[110:111], v[96:97], v[84:85] op_sel_hi:[0,1,1]
	v_med3_f32 v94, v94, s70, v167
	v_med3_f32 v95, v95, s70, v167
	v_pk_mul_f32 v[100:101], v[100:101], v[104:105]
	v_med3_f32 v92, v92, s73, v184
	v_pk_mul_f32 v[100:101], v[100:101], v[102:103]
	v_exp_f32_e64 v102, -v90
	v_exp_f32_e64 v103, -v91
	v_med3_f32 v93, v93, s73, v184
	v_pk_add_f32 v[102:103], v[102:103], 1.0 op_sel_hi:[1,0]
	s_nop 0
	s_nop 0
	s_nop 0
	v_pk_mul_f32 v[90:91], v[90:91], v[94:95]
	v_med3_f32 v94, v96, s70, v167
	v_med3_f32 v95, v97, s70, v167
	v_exp_f32_e64 v96, -v92
	v_exp_f32_e64 v97, -v93
	s_nop 0
	v_pk_add_f32 v[96:97], v[96:97], 1.0 op_sel_hi:[1,0]
	s_nop 0
	v_pk_mul_f32 v[180:181], v[102:103], v[96:97]
	v_rcp_f32_e32 v180, v180
	v_rcp_f32_e32 v181, v181
	s_nop 0
	v_pk_mul_f32 v[182:183], v[180:181], v[96:97]
	v_pk_mul_f32 v[96:97], v[180:181], v[102:103]
	v_pk_mul_f32 v[90:91], v[90:91], v[182:183]
	s_nop 0
	v_pk_mul_f32 v[92:93], v[92:93], v[96:97]
	s_nop 0
	v_pk_mul_f32 v[92:93], v[92:93], v[94:95]
	v_cvt_pk_fp8_f32 v95, v90, v91
	v_mul_f32_e32 v90, 0x3d800000, v174
	v_pk_fma_f32 v[74:75], v[90:91], v[74:75], v[150:151] op_sel_hi:[0,1,1]
	v_med3_f32 v74, v74, s73, v184
	v_med3_f32 v75, v75, s73, v184
	v_cvt_pk_fp8_f32 v95, v92, v93 op_sel:[0,0,1]
	v_exp_f32_e64 v92, -v74
	v_exp_f32_e64 v93, -v75
	v_pk_fma_f32 v[76:77], v[90:91], v[76:77], v[156:157] op_sel_hi:[0,1,1]
	v_pk_fma_f32 v[78:79], v[90:91], v[78:79], v[152:153] op_sel_hi:[0,1,1]
	v_pk_fma_f32 v[80:81], v[90:91], v[80:81], v[154:155] op_sel_hi:[0,1,1]
	v_pk_add_f32 v[92:93], v[92:93], 1.0 op_sel_hi:[1,0]
	v_med3_f32 v78, v78, s70, v167
	v_med3_f32 v79, v79, s70, v167
	v_med3_f32 v76, v76, s73, v184
	v_med3_f32 v77, v77, s73, v184
	v_pk_fma_f32 v[66:67], v[90:91], v[66:67], v[86:87] op_sel_hi:[0,1,1]
	v_pk_mul_f32 v[74:75], v[74:75], v[78:79]
	v_med3_f32 v78, v80, s70, v167
	v_med3_f32 v79, v81, s70, v167
	v_exp_f32_e64 v80, -v76
	v_exp_f32_e64 v81, -v77
	v_med3_f32 v66, v66, s73, v184
	v_med3_f32 v67, v67, s73, v184
	v_pk_fma_f32 v[68:69], v[90:91], v[68:69], v[88:89] op_sel_hi:[0,1,1]
	v_pk_add_f32 v[80:81], v[80:81], 1.0 op_sel_hi:[1,0]
	v_pk_fma_f32 v[70:71], v[90:91], v[70:71], v[82:83] op_sel_hi:[0,1,1]
	v_pk_mul_f32 v[180:181], v[92:93], v[80:81]
	v_rcp_f32_e32 v180, v180
	v_rcp_f32_e32 v181, v181
	s_nop 0
	v_pk_mul_f32 v[182:183], v[180:181], v[80:81]
	v_pk_mul_f32 v[80:81], v[180:181], v[92:93]
	v_pk_mul_f32 v[74:75], v[74:75], v[182:183]
	v_pk_fma_f32 v[72:73], v[90:91], v[72:73], v[84:85] op_sel_hi:[0,1,1]
	v_med3_f32 v70, v70, s70, v167
	v_med3_f32 v71, v71, s70, v167
	v_pk_mul_f32 v[76:77], v[76:77], v[80:81]
	v_med3_f32 v68, v68, s73, v184
	v_pk_mul_f32 v[76:77], v[76:77], v[78:79]
	v_exp_f32_e64 v78, -v66
	v_exp_f32_e64 v79, -v67
	v_med3_f32 v69, v69, s73, v184
	v_cvt_pk_fp8_f32 v94, v98, v99
	v_pk_add_f32 v[78:79], v[78:79], 1.0 op_sel_hi:[1,0]
	v_cvt_pk_fp8_f32 v94, v100, v101 op_sel:[0,0,1]
	ds_write_b64 v122, v[94:95]
	s_nop 0
	v_pk_mul_f32 v[66:67], v[66:67], v[70:71]
	v_med3_f32 v70, v72, s70, v167
	v_med3_f32 v71, v73, s70, v167
	v_exp_f32_e64 v72, -v68
	v_exp_f32_e64 v73, -v69
	s_nop 0
	v_pk_add_f32 v[72:73], v[72:73], 1.0 op_sel_hi:[1,0]
	s_nop 0
	v_pk_mul_f32 v[180:181], v[78:79], v[72:73]
	v_rcp_f32_e32 v180, v180
	v_rcp_f32_e32 v181, v181
	s_nop 0
	v_pk_mul_f32 v[182:183], v[180:181], v[72:73]
	v_pk_mul_f32 v[72:73], v[180:181], v[78:79]
	v_pk_mul_f32 v[66:67], v[66:67], v[182:183]
	s_nop 0
	v_pk_mul_f32 v[68:69], v[68:69], v[72:73]
	s_nop 0
	v_pk_mul_f32 v[68:69], v[68:69], v[70:71]
	v_cvt_pk_fp8_f32 v70, v74, v75
	v_cvt_pk_fp8_f32 v71, v66, v67
	v_cvt_pk_fp8_f32 v70, v76, v77 op_sel:[0,0,1]
	v_cvt_pk_fp8_f32 v71, v68, v69 op_sel:[0,0,1]
	ds_write_b64 v122, v[70:71] offset:768
	v_or_b32_e32 v70, 32, v106
	ds_read_b128 v[66:69], v108
	v_ashrrev_i32_e32 v71, 31, v70
	v_lshl_add_u32 v70, v70, 10, v142
	s_add_u32 s86, s16, s8
	s_addc_u32 s87, s17, s9
	s_waitcnt lgkmcnt(0)
	global_store_dwordx4 v70, v[66:69], s[86:87]
	s_nop 1
	v_mul_f32_e32 v66, 0x3d800000, v173
	v_pk_fma_f32 v[58:59], v[66:67], v[58:59], v[150:151] op_sel_hi:[0,1,1]
	v_med3_f32 v58, v58, s73, v184
	v_med3_f32 v59, v59, s73, v184
	v_exp_f32_e64 v68, -v58
	v_exp_f32_e64 v69, -v59
	v_pk_fma_f32 v[60:61], v[66:67], v[60:61], v[156:157] op_sel_hi:[0,1,1]
	v_pk_fma_f32 v[62:63], v[66:67], v[62:63], v[152:153] op_sel_hi:[0,1,1]
	v_pk_fma_f32 v[64:65], v[66:67], v[64:65], v[154:155] op_sel_hi:[0,1,1]
	v_pk_add_f32 v[68:69], v[68:69], 1.0 op_sel_hi:[1,0]
	v_med3_f32 v62, v62, s70, v167
	v_med3_f32 v63, v63, s70, v167
	v_med3_f32 v60, v60, s73, v184
	v_med3_f32 v61, v61, s73, v184
	v_pk_fma_f32 v[50:51], v[66:67], v[50:51], v[86:87] op_sel_hi:[0,1,1]
	v_pk_mul_f32 v[58:59], v[58:59], v[62:63]
	v_med3_f32 v62, v64, s70, v167
	v_med3_f32 v63, v65, s70, v167
	v_exp_f32_e64 v64, -v60
	v_exp_f32_e64 v65, -v61
	v_med3_f32 v50, v50, s73, v184
	v_med3_f32 v51, v51, s73, v184
	v_pk_fma_f32 v[52:53], v[66:67], v[52:53], v[88:89] op_sel_hi:[0,1,1]
	v_pk_add_f32 v[64:65], v[64:65], 1.0 op_sel_hi:[1,0]
	v_pk_fma_f32 v[54:55], v[66:67], v[54:55], v[82:83] op_sel_hi:[0,1,1]
	v_pk_mul_f32 v[180:181], v[68:69], v[64:65]
	v_rcp_f32_e32 v180, v180
	v_rcp_f32_e32 v181, v181
	s_nop 0
	v_pk_mul_f32 v[182:183], v[180:181], v[64:65]
	v_pk_mul_f32 v[64:65], v[180:181], v[68:69]
	v_pk_mul_f32 v[58:59], v[58:59], v[182:183]
	v_pk_fma_f32 v[56:57], v[66:67], v[56:57], v[84:85] op_sel_hi:[0,1,1]
	v_med3_f32 v54, v54, s70, v167
	v_med3_f32 v55, v55, s70, v167
	v_pk_mul_f32 v[60:61], v[60:61], v[64:65]
	v_med3_f32 v52, v52, s73, v184
	v_pk_mul_f32 v[60:61], v[60:61], v[62:63]
	v_exp_f32_e64 v62, -v50
	v_exp_f32_e64 v63, -v51
	v_med3_f32 v53, v53, s73, v184
	v_pk_add_f32 v[62:63], v[62:63], 1.0 op_sel_hi:[1,0]
	s_nop 0
	s_nop 0
	s_nop 0
	v_pk_mul_f32 v[50:51], v[50:51], v[54:55]
	v_med3_f32 v54, v56, s70, v167
	v_med3_f32 v55, v57, s70, v167
	v_exp_f32_e64 v56, -v52
	v_exp_f32_e64 v57, -v53
	s_nop 0
	v_pk_add_f32 v[56:57], v[56:57], 1.0 op_sel_hi:[1,0]
	s_nop 0
	v_pk_mul_f32 v[180:181], v[62:63], v[56:57]
	v_rcp_f32_e32 v180, v180
	v_rcp_f32_e32 v181, v181
	s_nop 0
	v_pk_mul_f32 v[182:183], v[180:181], v[56:57]
	v_pk_mul_f32 v[56:57], v[180:181], v[62:63]
	v_pk_mul_f32 v[50:51], v[50:51], v[182:183]
	s_nop 0
	v_pk_mul_f32 v[52:53], v[52:53], v[56:57]
	s_nop 0
	v_pk_mul_f32 v[52:53], v[52:53], v[54:55]
	v_cvt_pk_fp8_f32 v55, v50, v51
	v_mul_f32_e32 v50, 0x3d800000, v172
	v_pk_fma_f32 v[42:43], v[50:51], v[42:43], v[150:151] op_sel_hi:[0,1,1]
	v_med3_f32 v42, v42, s73, v184
	v_med3_f32 v43, v43, s73, v184
	v_cvt_pk_fp8_f32 v55, v52, v53 op_sel:[0,0,1]
	v_exp_f32_e64 v52, -v42
	v_exp_f32_e64 v53, -v43
	v_pk_fma_f32 v[44:45], v[50:51], v[44:45], v[156:157] op_sel_hi:[0,1,1]
	v_pk_fma_f32 v[46:47], v[50:51], v[46:47], v[152:153] op_sel_hi:[0,1,1]
	v_pk_fma_f32 v[48:49], v[50:51], v[48:49], v[154:155] op_sel_hi:[0,1,1]
	v_pk_add_f32 v[52:53], v[52:53], 1.0 op_sel_hi:[1,0]
	v_med3_f32 v46, v46, s70, v167
	v_med3_f32 v47, v47, s70, v167
	v_med3_f32 v44, v44, s73, v184
	v_med3_f32 v45, v45, s73, v184
	v_pk_fma_f32 v[34:35], v[50:51], v[34:35], v[86:87] op_sel_hi:[0,1,1]
	v_pk_mul_f32 v[42:43], v[42:43], v[46:47]
	v_med3_f32 v46, v48, s70, v167
	v_med3_f32 v47, v49, s70, v167
	v_exp_f32_e64 v48, -v44
	v_exp_f32_e64 v49, -v45
	v_med3_f32 v34, v34, s73, v184
	v_med3_f32 v35, v35, s73, v184
	v_pk_fma_f32 v[36:37], v[50:51], v[36:37], v[88:89] op_sel_hi:[0,1,1]
	v_pk_add_f32 v[48:49], v[48:49], 1.0 op_sel_hi:[1,0]
	v_pk_fma_f32 v[38:39], v[50:51], v[38:39], v[82:83] op_sel_hi:[0,1,1]
	v_pk_mul_f32 v[180:181], v[52:53], v[48:49]
	v_rcp_f32_e32 v180, v180
	v_rcp_f32_e32 v181, v181
	s_nop 0
	v_pk_mul_f32 v[182:183], v[180:181], v[48:49]
	v_pk_mul_f32 v[48:49], v[180:181], v[52:53]
	v_pk_mul_f32 v[42:43], v[42:43], v[182:183]
	v_pk_fma_f32 v[40:41], v[50:51], v[40:41], v[84:85] op_sel_hi:[0,1,1]
	v_med3_f32 v38, v38, s70, v167
	v_med3_f32 v39, v39, s70, v167
	v_pk_mul_f32 v[44:45], v[44:45], v[48:49]
	v_med3_f32 v36, v36, s73, v184
	v_pk_mul_f32 v[44:45], v[44:45], v[46:47]
	v_exp_f32_e64 v46, -v34
	v_exp_f32_e64 v47, -v35
	v_med3_f32 v37, v37, s73, v184
	v_cvt_pk_fp8_f32 v54, v58, v59
	v_pk_add_f32 v[46:47], v[46:47], 1.0 op_sel_hi:[1,0]
	v_cvt_pk_fp8_f32 v54, v60, v61 op_sel:[0,0,1]
	ds_write_b64 v122, v[54:55]
	s_nop 0
	v_pk_mul_f32 v[34:35], v[34:35], v[38:39]
	v_med3_f32 v38, v40, s70, v167
	v_med3_f32 v39, v41, s70, v167
	v_exp_f32_e64 v40, -v36
	v_exp_f32_e64 v41, -v37
	s_nop 0
	v_pk_add_f32 v[40:41], v[40:41], 1.0 op_sel_hi:[1,0]
	s_nop 0
	v_pk_mul_f32 v[180:181], v[46:47], v[40:41]
	v_rcp_f32_e32 v180, v180
	v_rcp_f32_e32 v181, v181
	s_nop 0
	v_pk_mul_f32 v[182:183], v[180:181], v[40:41]
	v_pk_mul_f32 v[40:41], v[180:181], v[46:47]
	v_pk_mul_f32 v[34:35], v[34:35], v[182:183]
	s_nop 0
	v_pk_mul_f32 v[36:37], v[36:37], v[40:41]
	s_nop 0
	v_pk_mul_f32 v[36:37], v[36:37], v[38:39]
	v_cvt_pk_fp8_f32 v38, v42, v43
	v_cvt_pk_fp8_f32 v39, v34, v35
	v_cvt_pk_fp8_f32 v38, v44, v45 op_sel:[0,0,1]
	v_cvt_pk_fp8_f32 v39, v36, v37 op_sel:[0,0,1]
	ds_write_b64 v122, v[38:39] offset:768
	v_add_u32_e32 v38, 0x80, v106
	ds_read_b128 v[34:37], v108
	v_ashrrev_i32_e32 v39, 31, v38
	v_lshl_add_u32 v38, v38, 10, v142
	s_add_u32 s86, s16, s8
	s_addc_u32 s87, s17, s9
	s_waitcnt lgkmcnt(0)
	global_store_dwordx4 v38, v[34:37], s[86:87]
	s_nop 1
	v_mul_f32_e32 v34, 0x3d800000, v171
	v_pk_fma_f32 v[26:27], v[34:35], v[26:27], v[150:151] op_sel_hi:[0,1,1]
	v_med3_f32 v26, v26, s73, v184
	v_med3_f32 v27, v27, s73, v184
	v_exp_f32_e64 v36, -v26
	v_exp_f32_e64 v37, -v27
	v_pk_fma_f32 v[28:29], v[34:35], v[28:29], v[156:157] op_sel_hi:[0,1,1]
	v_pk_fma_f32 v[30:31], v[34:35], v[30:31], v[152:153] op_sel_hi:[0,1,1]
	v_pk_fma_f32 v[32:33], v[34:35], v[32:33], v[154:155] op_sel_hi:[0,1,1]
	v_pk_add_f32 v[36:37], v[36:37], 1.0 op_sel_hi:[1,0]
	v_med3_f32 v30, v30, s70, v167
	v_med3_f32 v31, v31, s70, v167
	v_med3_f32 v28, v28, s73, v184
	v_med3_f32 v29, v29, s73, v184
	v_pk_fma_f32 v[18:19], v[34:35], v[18:19], v[86:87] op_sel_hi:[0,1,1]
	v_pk_mul_f32 v[26:27], v[26:27], v[30:31]
	v_med3_f32 v30, v32, s70, v167
	v_med3_f32 v31, v33, s70, v167
	v_exp_f32_e64 v32, -v28
	v_exp_f32_e64 v33, -v29
	v_med3_f32 v18, v18, s73, v184
	v_med3_f32 v19, v19, s73, v184
	v_pk_fma_f32 v[20:21], v[34:35], v[20:21], v[88:89] op_sel_hi:[0,1,1]
	v_pk_add_f32 v[32:33], v[32:33], 1.0 op_sel_hi:[1,0]
	v_pk_fma_f32 v[22:23], v[34:35], v[22:23], v[82:83] op_sel_hi:[0,1,1]
	v_pk_mul_f32 v[180:181], v[36:37], v[32:33]
	v_rcp_f32_e32 v180, v180
	v_rcp_f32_e32 v181, v181
	s_nop 0
	v_pk_mul_f32 v[182:183], v[180:181], v[32:33]
	v_pk_mul_f32 v[32:33], v[180:181], v[36:37]
	v_pk_mul_f32 v[26:27], v[26:27], v[182:183]
	v_pk_fma_f32 v[24:25], v[34:35], v[24:25], v[84:85] op_sel_hi:[0,1,1]
	v_med3_f32 v22, v22, s70, v167
	v_med3_f32 v23, v23, s70, v167
	v_pk_mul_f32 v[28:29], v[28:29], v[32:33]
	v_med3_f32 v20, v20, s73, v184
	v_pk_mul_f32 v[28:29], v[28:29], v[30:31]
	v_exp_f32_e64 v30, -v18
	v_exp_f32_e64 v31, -v19
	v_med3_f32 v21, v21, s73, v184
	v_pk_add_f32 v[30:31], v[30:31], 1.0 op_sel_hi:[1,0]
	s_nop 0
	s_nop 0
	s_nop 0
	v_pk_mul_f32 v[18:19], v[18:19], v[22:23]
	v_med3_f32 v22, v24, s70, v167
	v_med3_f32 v23, v25, s70, v167
	v_exp_f32_e64 v24, -v20
	v_exp_f32_e64 v25, -v21
	s_nop 0
	v_pk_add_f32 v[24:25], v[24:25], 1.0 op_sel_hi:[1,0]
	s_nop 0
	v_pk_mul_f32 v[180:181], v[30:31], v[24:25]
	v_rcp_f32_e32 v180, v180
	v_rcp_f32_e32 v181, v181
	s_nop 0
	v_pk_mul_f32 v[182:183], v[180:181], v[24:25]
	v_pk_mul_f32 v[24:25], v[180:181], v[30:31]
	v_pk_mul_f32 v[18:19], v[18:19], v[182:183]
	s_nop 0
	v_pk_mul_f32 v[20:21], v[20:21], v[24:25]
	s_nop 0
	v_pk_mul_f32 v[20:21], v[20:21], v[22:23]
	v_cvt_pk_fp8_f32 v23, v18, v19
	v_mul_f32_e32 v18, 0x3d800000, v168
	v_pk_fma_f32 v[10:11], v[18:19], v[10:11], v[150:151] op_sel_hi:[0,1,1]
	v_med3_f32 v10, v10, s73, v184
	v_med3_f32 v11, v11, s73, v184
	v_cvt_pk_fp8_f32 v23, v20, v21 op_sel:[0,0,1]
	v_exp_f32_e64 v20, -v10
	v_exp_f32_e64 v21, -v11
	v_pk_fma_f32 v[12:13], v[18:19], v[12:13], v[156:157] op_sel_hi:[0,1,1]
	v_pk_fma_f32 v[14:15], v[18:19], v[14:15], v[152:153] op_sel_hi:[0,1,1]
	v_pk_fma_f32 v[16:17], v[18:19], v[16:17], v[154:155] op_sel_hi:[0,1,1]
	v_pk_add_f32 v[20:21], v[20:21], 1.0 op_sel_hi:[1,0]
	v_med3_f32 v14, v14, s70, v167
	v_med3_f32 v15, v15, s70, v167
	v_med3_f32 v12, v12, s73, v184
	v_med3_f32 v13, v13, s73, v184
	v_pk_fma_f32 v[2:3], v[18:19], v[2:3], v[86:87] op_sel_hi:[0,1,1]
	v_pk_mul_f32 v[10:11], v[10:11], v[14:15]
	v_med3_f32 v14, v16, s70, v167
	v_med3_f32 v15, v17, s70, v167
	v_exp_f32_e64 v16, -v12
	v_exp_f32_e64 v17, -v13
	v_med3_f32 v2, v2, s73, v184
	v_med3_f32 v3, v3, s73, v184
	v_pk_fma_f32 v[4:5], v[18:19], v[4:5], v[88:89] op_sel_hi:[0,1,1]
	v_pk_add_f32 v[16:17], v[16:17], 1.0 op_sel_hi:[1,0]
	v_pk_fma_f32 v[6:7], v[18:19], v[6:7], v[82:83] op_sel_hi:[0,1,1]
	v_pk_mul_f32 v[180:181], v[20:21], v[16:17]
	v_rcp_f32_e32 v180, v180
	v_rcp_f32_e32 v181, v181
	s_nop 0
	v_pk_mul_f32 v[182:183], v[180:181], v[16:17]
	v_pk_mul_f32 v[16:17], v[180:181], v[20:21]
	v_pk_mul_f32 v[10:11], v[10:11], v[182:183]
	v_pk_fma_f32 v[8:9], v[18:19], v[8:9], v[84:85] op_sel_hi:[0,1,1]
	v_med3_f32 v6, v6, s70, v167
	v_med3_f32 v7, v7, s70, v167
	v_pk_mul_f32 v[12:13], v[12:13], v[16:17]
	v_med3_f32 v4, v4, s73, v184
	v_pk_mul_f32 v[12:13], v[12:13], v[14:15]
	v_exp_f32_e64 v14, -v2
	v_exp_f32_e64 v15, -v3
	v_med3_f32 v5, v5, s73, v184
	v_cvt_pk_fp8_f32 v22, v26, v27
	v_pk_add_f32 v[14:15], v[14:15], 1.0 op_sel_hi:[1,0]
	v_cvt_pk_fp8_f32 v22, v28, v29 op_sel:[0,0,1]
	ds_write_b64 v122, v[22:23]
	s_nop 0
	v_pk_mul_f32 v[2:3], v[2:3], v[6:7]
	v_med3_f32 v6, v8, s70, v167
	v_med3_f32 v7, v9, s70, v167
	v_exp_f32_e64 v8, -v4
	v_exp_f32_e64 v9, -v5
	s_nop 0
	v_pk_add_f32 v[8:9], v[8:9], 1.0 op_sel_hi:[1,0]
	s_nop 0
	v_pk_mul_f32 v[180:181], v[14:15], v[8:9]
	v_rcp_f32_e32 v180, v180
	v_rcp_f32_e32 v181, v181
	s_nop 0
	v_pk_mul_f32 v[182:183], v[180:181], v[8:9]
	v_pk_mul_f32 v[8:9], v[180:181], v[14:15]
	v_pk_mul_f32 v[2:3], v[2:3], v[182:183]
	s_nop 0
	v_pk_mul_f32 v[4:5], v[4:5], v[8:9]
	s_nop 0
	v_pk_mul_f32 v[4:5], v[4:5], v[6:7]
	v_cvt_pk_fp8_f32 v6, v10, v11
	v_cvt_pk_fp8_f32 v7, v2, v3
	v_cvt_pk_fp8_f32 v6, v12, v13 op_sel:[0,0,1]
	v_cvt_pk_fp8_f32 v7, v4, v5 op_sel:[0,0,1]
	ds_write_b64 v122, v[6:7] offset:768
	v_add_u32_e32 v6, 0xa0, v106
	ds_read_b128 v[2:5], v108
	v_ashrrev_i32_e32 v7, 31, v6
	v_lshl_add_u32 v6, v6, 10, v142
	s_add_u32 s86, s16, s8
	s_addc_u32 s87, s17, s9
	s_mov_b64 s[8:9], -1
	s_waitcnt lgkmcnt(0)
	global_store_dwordx4 v6, v[2:5], s[86:87]
	s_cbranch_vccnz .LBB0_1537
	s_lshl_b64 s[6:7], s[74:75], 12
	s_add_u32 s9, s33, s6
	s_addc_u32 s69, s54, s7
	s_lshl_b32 s6, s68, 7
	s_ashr_i32 s7, s6, 31
	v_mov_b32_e32 v2, v0
	s_lshl_b64 s[6:7], s[6:7], 1
	s_add_u32 s6, s9, s6
	v_readfirstlane_b32 s8, v2
	s_addc_u32 s7, s69, s7
	s_and_b32 s9, s8, 0xc0
	s_add_u32 s6, s6, s9
	s_addc_u32 s7, s7, 0
	v_and_b32_e32 v3, 48, v2
	global_load_dwordx4 v[86:89], v3, s[6:7]
	global_load_dwordx4 v[82:85], v3, s[6:7] offset:2048
	s_ashr_i32 s7, s8, 2
	s_lshl_b32 s6, s72, 8
	s_andn2_b32 s7, s7, 63
	s_add_i32 s7, s7, s6
	v_and_or_b32 v2, v2, 15, s7
	v_lshlrev_b32_e32 v4, 2, v2
	global_load_dword v177, v4, s[12:13] offset:0
	global_load_dword v176, v4, s[12:13] offset:64
	global_load_dword v175, v4, s[12:13] offset:128
	global_load_dword v174, v4, s[12:13] offset:192
	global_load_dword v173, v4, s[12:13] offset:512
	global_load_dword v172, v4, s[12:13] offset:576
	global_load_dword v171, v4, s[12:13] offset:640
	global_load_dword v168, v4, s[12:13] offset:704
	s_andn2_b64 vcc, exec, s[14:15]
	s_cbranch_vccnz .LBB0_1536
	s_barrier
	s_branch .LBB0_1536

.LBB0_1627:
	v_lshlrev_b32_e32 v158, 16, v6
	v_and_b32_e32 v159, 0xffff0000, v6
	v_lshlrev_b32_e32 v154, 16, v8
	v_and_b32_e32 v155, 0xffff0000, v8
	v_lshlrev_b32_e32 v156, 16, v7
	v_and_b32_e32 v157, 0xffff0000, v7
	v_lshlrev_b32_e32 v152, 16, v9
	v_and_b32_e32 v153, 0xffff0000, v9
	s_waitcnt vmcnt(10)
	v_lshlrev_b32_e32 v6, 16, v4
	v_and_b32_e32 v7, 0xffff0000, v4
	v_mul_f32_e32 v4, 0x41000000, v146
	v_pk_fma_f32 v[134:135], v[134:135], s[36:37], v[158:159] op_sel_hi:[1,0,1]
	v_pk_fma_f32 v[130:131], v[130:131], s[36:37], v[154:155] op_sel_hi:[1,0,1]
	v_pk_fma_f32 v[136:137], v[136:137], s[36:37], v[156:157] op_sel_hi:[1,0,1]
	v_pk_mul_f32 v[134:135], v[4:5], v[134:135] op_sel_hi:[0,1]
	v_pk_fma_f32 v[132:133], v[132:133], s[36:37], v[152:153] op_sel_hi:[1,0,1]
	v_pk_mul_f32 v[130:131], v[4:5], v[130:131] op_sel_hi:[0,1]
	v_lshlrev_b32_e32 v150, 16, v2
	v_and_b32_e32 v151, 0xffff0000, v2
	v_lshlrev_b32_e32 v8, 16, v3
	v_and_b32_e32 v9, 0xffff0000, v3
	v_lshlrev_b32_e32 v2, 16, v5
	v_and_b32_e32 v3, 0xffff0000, v5
	v_pk_mul_f32 v[136:137], v[4:5], v[136:137] op_sel_hi:[0,1]
	v_pk_mul_f32 v[132:133], v[4:5], v[132:133] op_sel_hi:[0,1]
	v_med3_f32 v5, v134, s70, v164
	v_med3_f32 v134, v130, s70, v164
	v_med3_f32 v135, v135, s70, v164
	v_cvt_pk_fp8_f32 v130, v5, v135
	v_med3_f32 v136, v136, s70, v164
	v_med3_f32 v5, v137, s70, v164
	v_pk_fma_f32 v[126:127], v[126:127], s[36:37], v[150:151] op_sel_hi:[1,0,1]
	v_pk_fma_f32 v[128:129], v[128:129], s[36:37], v[8:9] op_sel_hi:[1,0,1]
	v_pk_fma_f32 v[122:123], v[122:123], s[36:37], v[6:7] op_sel_hi:[1,0,1]
	v_pk_fma_f32 v[124:125], v[124:125], s[36:37], v[2:3] op_sel_hi:[1,0,1]
	v_cvt_pk_fp8_f32 v130, v136, v5 op_sel:[0,0,1]
	v_pk_mul_f32 v[128:129], v[4:5], v[128:129] op_sel_hi:[0,1]
	v_pk_mul_f32 v[126:127], v[4:5], v[126:127] op_sel_hi:[0,1]
	v_pk_mul_f32 v[124:125], v[4:5], v[124:125] op_sel_hi:[0,1]
	v_pk_mul_f32 v[4:5], v[4:5], v[122:123] op_sel_hi:[0,1]
	v_med3_f32 v146, v131, s70, v164
	v_med3_f32 v122, v126, s70, v164
	v_med3_f32 v123, v4, s70, v164
	v_med3_f32 v126, v127, s70, v164
	v_med3_f32 v127, v5, s70, v164
	v_cvt_pk_fp8_f32 v131, v134, v146
	v_cvt_pk_fp8_f32 v4, v122, v126
	v_cvt_pk_fp8_f32 v5, v123, v127
	v_mov_b32_e32 v171, v0
	v_med3_f32 v132, v132, s70, v164
	v_readfirstlane_b32 s39, v171
	s_lshr_b32 s6, s39, 6
	v_med3_f32 v133, v133, s70, v164
	v_med3_f32 v128, v128, s70, v164
	v_med3_f32 v124, v124, s70, v164
	v_med3_f32 v122, v129, s70, v164
	v_med3_f32 v123, v125, s70, v164
	s_mulk_i32 s6, 0xb00
	v_cvt_pk_fp8_f32 v131, v132, v133 op_sel:[0,0,1]
	v_cvt_pk_fp8_f32 v4, v128, v122 op_sel:[0,0,1]
	v_cvt_pk_fp8_f32 v5, v124, v123 op_sel:[0,0,1]
	s_add_i32 s6, s6, 0
	v_and_b32_e32 v172, 15, v171
	v_lshrrev_b32_e32 v123, 1, v171
	s_add_i32 s41, s6, 0x20000
	v_mul_u32_u24_e32 v122, 0x50, v172
	v_and_b32_e32 v123, 24, v123
	v_add3_u32 v122, s41, v122, v123
	s_and_b32 s7, s39, 0xc0
	ds_write2_b64 v122, v[130:131], v[4:5] offset1:4
	v_bfe_u32 v4, v171, 2, 4
	s_ashr_i32 s39, s39, 2
	v_mul_u32_u24_e32 v5, 0x50, v4
	v_lshlrev_b32_e32 v123, 4, v171
	s_andn2_b32 s39, s39, 63
	v_lshl_or_b32 v4, s48, 8, v4
	v_and_b32_e32 v146, 48, v123
	v_add_u32_e32 v4, s39, v4
	v_mul_f32_e32 v130, 0x41000000, v170
	v_pk_fma_f32 v[118:119], v[118:119], s[36:37], v[158:159] op_sel_hi:[1,0,1]
	v_pk_fma_f32 v[114:115], v[114:115], s[36:37], v[154:155] op_sel_hi:[1,0,1]
	v_add3_u32 v123, s41, v5, v146
	v_ashrrev_i32_e32 v5, 31, v4
	v_pk_mul_f32 v[118:119], v[130:131], v[118:119] op_sel_hi:[0,1]
	v_pk_mul_f32 v[114:115], v[130:131], v[114:115] op_sel_hi:[0,1]
	v_lshl_add_u32 v128, v4, 10, v146
	v_med3_f32 v5, v118, s70, v164
	v_med3_f32 v118, v114, s70, v164
	v_med3_f32 v119, v119, s70, v164
	v_cvt_pk_fp8_f32 v114, v5, v119
	v_pk_fma_f32 v[120:121], v[120:121], s[36:37], v[156:157] op_sel_hi:[1,0,1]
	v_pk_fma_f32 v[116:117], v[116:117], s[36:37], v[152:153] op_sel_hi:[1,0,1]
	v_pk_mul_f32 v[120:121], v[130:131], v[120:121] op_sel_hi:[0,1]
	v_pk_mul_f32 v[116:117], v[130:131], v[116:117] op_sel_hi:[0,1]
	v_med3_f32 v131, v115, s70, v164
	v_pk_fma_f32 v[110:111], v[110:111], s[36:37], v[150:151] op_sel_hi:[1,0,1]
	v_pk_fma_f32 v[106:107], v[106:107], s[36:37], v[6:7] op_sel_hi:[1,0,1]
	v_med3_f32 v120, v120, s70, v164
	v_med3_f32 v5, v121, s70, v164
	v_pk_mul_f32 v[110:111], v[130:131], v[110:111] op_sel_hi:[0,1]
	v_pk_mul_f32 v[106:107], v[130:131], v[106:107] op_sel_hi:[0,1]
	v_cvt_pk_fp8_f32 v114, v120, v5 op_sel:[0,0,1]
	v_med3_f32 v5, v110, s70, v164
	v_med3_f32 v110, v106, s70, v164
	v_med3_f32 v111, v111, s70, v164
	v_cvt_pk_fp8_f32 v106, v5, v111
	v_pk_fma_f32 v[112:113], v[112:113], s[36:37], v[8:9] op_sel_hi:[1,0,1]
	v_pk_mul_f32 v[112:113], v[130:131], v[112:113] op_sel_hi:[0,1]
	v_med3_f32 v112, v112, s70, v164
	v_med3_f32 v5, v113, s70, v164
	v_cvt_pk_fp8_f32 v106, v112, v5 op_sel:[0,0,1]
	v_mul_f32_e32 v112, 0x41000000, v169
	v_pk_fma_f32 v[102:103], v[102:103], s[36:37], v[158:159] op_sel_hi:[1,0,1]
	v_pk_fma_f32 v[98:99], v[98:99], s[36:37], v[154:155] op_sel_hi:[1,0,1]
	v_cvt_pk_fp8_f32 v115, v118, v131
	v_pk_mul_f32 v[102:103], v[112:113], v[102:103] op_sel_hi:[0,1]
	v_pk_mul_f32 v[98:99], v[112:113], v[98:99] op_sel_hi:[0,1]
	v_med3_f32 v5, v102, s70, v164
	v_med3_f32 v102, v98, s70, v164
	v_med3_f32 v103, v103, s70, v164
	v_cvt_pk_fp8_f32 v98, v5, v103
	v_med3_f32 v116, v116, s70, v164
	v_med3_f32 v117, v117, s70, v164
	v_pk_fma_f32 v[104:105], v[104:105], s[36:37], v[156:157] op_sel_hi:[1,0,1]
	v_pk_fma_f32 v[100:101], v[100:101], s[36:37], v[152:153] op_sel_hi:[1,0,1]
	v_cvt_pk_fp8_f32 v115, v116, v117 op_sel:[0,0,1]
	v_med3_f32 v116, v107, s70, v164
	v_pk_mul_f32 v[104:105], v[112:113], v[104:105] op_sel_hi:[0,1]
	v_pk_mul_f32 v[100:101], v[112:113], v[100:101] op_sel_hi:[0,1]
	v_med3_f32 v113, v99, s70, v164
	v_pk_fma_f32 v[94:95], v[94:95], s[36:37], v[150:151] op_sel_hi:[1,0,1]
	v_pk_fma_f32 v[90:91], v[90:91], s[36:37], v[6:7] op_sel_hi:[1,0,1]
	v_cvt_pk_fp8_f32 v107, v110, v116
	v_med3_f32 v104, v104, s70, v164
	v_med3_f32 v5, v105, s70, v164
	v_pk_mul_f32 v[94:95], v[112:113], v[94:95] op_sel_hi:[0,1]
	v_pk_mul_f32 v[90:91], v[112:113], v[90:91] op_sel_hi:[0,1]
	v_pk_fma_f32 v[108:109], v[108:109], s[36:37], v[2:3] op_sel_hi:[1,0,1]
	v_cvt_pk_fp8_f32 v98, v104, v5 op_sel:[0,0,1]
	v_med3_f32 v5, v94, s70, v164
	v_med3_f32 v94, v90, s70, v164
	v_med3_f32 v95, v95, s70, v164
	s_lshl_b32 s6, s50, 8
	ds_read_b128 v[124:127], v123
	v_pk_mul_f32 v[108:109], v[130:131], v[108:109] op_sel_hi:[0,1]
	v_cvt_pk_fp8_f32 v99, v102, v113
	v_cvt_pk_fp8_f32 v90, v5, v95
	s_or_b32 s6, s7, s6
	v_med3_f32 v108, v108, s70, v164
	v_med3_f32 v109, v109, s70, v164
	v_pk_fma_f32 v[96:97], v[96:97], s[36:37], v[8:9] op_sel_hi:[1,0,1]
	s_ashr_i32 s7, s6, 31
	v_cvt_pk_fp8_f32 v107, v108, v109 op_sel:[0,0,1]
	v_pk_mul_f32 v[96:97], v[112:113], v[96:97] op_sel_hi:[0,1]
	s_add_u32 s86, s16, s6
	s_addc_u32 s87, s17, s7
	v_med3_f32 v100, v100, s70, v164
	v_med3_f32 v101, v101, s70, v164
	v_med3_f32 v96, v96, s70, v164
	v_med3_f32 v5, v97, s70, v164
	v_mov_b32_e32 v108, v128
	v_cvt_pk_fp8_f32 v99, v100, v101 op_sel:[0,0,1]
	v_med3_f32 v100, v91, s70, v164
	v_cvt_pk_fp8_f32 v90, v96, v5 op_sel:[0,0,1]
	v_mul_f32_e32 v96, 0x41000000, v168
	v_pk_fma_f32 v[78:79], v[78:79], s[36:37], v[158:159] op_sel_hi:[1,0,1]
	v_pk_fma_f32 v[74:75], v[74:75], s[36:37], v[154:155] op_sel_hi:[1,0,1]
	s_waitcnt lgkmcnt(0)
	global_store_dwordx4 v108, v[124:127], s[86:87]
	v_cvt_pk_fp8_f32 v91, v94, v100
	v_pk_fma_f32 v[80:81], v[80:81], s[36:37], v[156:157] op_sel_hi:[1,0,1]
	v_pk_mul_f32 v[78:79], v[96:97], v[78:79] op_sel_hi:[0,1]
	v_pk_fma_f32 v[76:77], v[76:77], s[36:37], v[152:153] op_sel_hi:[1,0,1]
	v_pk_mul_f32 v[74:75], v[96:97], v[74:75] op_sel_hi:[0,1]
	ds_write2_b64 v122, v[114:115], v[106:107] offset1:4
	v_or_b32_e32 v110, 16, v4
	v_pk_fma_f32 v[92:93], v[92:93], s[36:37], v[2:3] op_sel_hi:[1,0,1]
	v_pk_mul_f32 v[80:81], v[96:97], v[80:81] op_sel_hi:[0,1]
	v_pk_mul_f32 v[76:77], v[96:97], v[76:77] op_sel_hi:[0,1]
	v_med3_f32 v5, v78, s70, v164
	v_med3_f32 v78, v74, s70, v164
	v_med3_f32 v79, v79, s70, v164
	v_med3_f32 v97, v75, s70, v164
	ds_read_b128 v[106:109], v123
	v_ashrrev_i32_e32 v111, 31, v110
	v_pk_mul_f32 v[92:93], v[112:113], v[92:93] op_sel_hi:[0,1]
	v_cvt_pk_fp8_f32 v74, v5, v79
	v_cvt_pk_fp8_f32 v75, v78, v97
	v_lshl_add_u32 v110, v110, 10, v146
	v_med3_f32 v92, v92, s70, v164
	v_med3_f32 v93, v93, s70, v164
	v_cvt_pk_fp8_f32 v91, v92, v93 op_sel:[0,0,1]
	v_pk_fma_f32 v[62:63], v[62:63], s[36:37], v[150:151] op_sel_hi:[1,0,1]
	v_pk_fma_f32 v[58:59], v[58:59], s[36:37], v[6:7] op_sel_hi:[1,0,1]
	s_add_u32 s86, s16, s6
	s_addc_u32 s87, s17, s7
	v_med3_f32 v80, v80, s70, v164
	v_med3_f32 v76, v76, s70, v164
	v_med3_f32 v5, v81, s70, v164
	v_med3_f32 v77, v77, s70, v164
	v_pk_mul_f32 v[62:63], v[96:97], v[62:63] op_sel_hi:[0,1]
	v_pk_mul_f32 v[58:59], v[96:97], v[58:59] op_sel_hi:[0,1]
	v_mov_b32_e32 v92, v110
	v_cvt_pk_fp8_f32 v74, v80, v5 op_sel:[0,0,1]
	v_cvt_pk_fp8_f32 v75, v76, v77 op_sel:[0,0,1]
	v_med3_f32 v5, v62, s70, v164
	v_med3_f32 v62, v58, s70, v164
	v_med3_f32 v63, v63, s70, v164
	v_med3_f32 v76, v59, s70, v164
	s_waitcnt lgkmcnt(0)
	global_store_dwordx4 v92, v[106:109], s[86:87]
	v_cvt_pk_fp8_f32 v58, v5, v63
	v_cvt_pk_fp8_f32 v59, v62, v76
	ds_write2_b64 v122, v[98:99], v[90:91] offset1:4
	v_or_b32_e32 v94, 32, v4
	v_pk_fma_f32 v[64:65], v[64:65], s[36:37], v[8:9] op_sel_hi:[1,0,1]
	v_pk_fma_f32 v[60:61], v[60:61], s[36:37], v[2:3] op_sel_hi:[1,0,1]
	ds_read_b128 v[90:93], v123
	v_ashrrev_i32_e32 v95, 31, v94
	v_pk_mul_f32 v[64:65], v[96:97], v[64:65] op_sel_hi:[0,1]
	v_pk_mul_f32 v[60:61], v[96:97], v[60:61] op_sel_hi:[0,1]
	v_lshl_add_u32 v94, v94, 10, v146
	v_med3_f32 v64, v64, s70, v164
	v_med3_f32 v60, v60, s70, v164
	v_med3_f32 v5, v65, s70, v164
	v_med3_f32 v61, v61, s70, v164
	v_cvt_pk_fp8_f32 v58, v64, v5 op_sel:[0,0,1]
	v_cvt_pk_fp8_f32 v59, v60, v61 op_sel:[0,0,1]
	s_add_u32 s86, s16, s6
	s_addc_u32 s87, s17, s7
	v_mov_b32_e32 v60, v94
	s_waitcnt lgkmcnt(0)
	global_store_dwordx4 v60, v[90:93], s[86:87]
	ds_write2_b64 v122, v[74:75], v[58:59] offset1:4
	v_mul_f32_e32 v64, 0x41000000, v167
	v_pk_fma_f32 v[74:75], v[86:87], s[36:37], v[158:159] op_sel_hi:[1,0,1]
	v_pk_fma_f32 v[78:79], v[82:83], s[36:37], v[154:155] op_sel_hi:[1,0,1]
	v_pk_mul_f32 v[74:75], v[64:65], v[74:75] op_sel_hi:[0,1]
	v_pk_fma_f32 v[76:77], v[88:89], s[36:37], v[156:157] op_sel_hi:[1,0,1]
	v_pk_fma_f32 v[80:81], v[84:85], s[36:37], v[152:153] op_sel_hi:[1,0,1]
	v_pk_mul_f32 v[78:79], v[64:65], v[78:79] op_sel_hi:[0,1]
	v_med3_f32 v5, v74, s70, v164
	v_med3_f32 v75, v75, s70, v164
	v_pk_mul_f32 v[76:77], v[64:65], v[76:77] op_sel_hi:[0,1]
	v_pk_mul_f32 v[80:81], v[64:65], v[80:81] op_sel_hi:[0,1]
	v_med3_f32 v65, v78, s70, v164
	v_med3_f32 v78, v79, s70, v164
	v_cvt_pk_fp8_f32 v74, v5, v75
	v_cvt_pk_fp8_f32 v75, v65, v78
	v_med3_f32 v79, v80, s70, v164
	v_med3_f32 v65, v81, s70, v164
	v_pk_fma_f32 v[70:71], v[70:71], s[36:37], v[150:151] op_sel_hi:[1,0,1]
	v_pk_fma_f32 v[72:73], v[72:73], s[36:37], v[8:9] op_sel_hi:[1,0,1]
	v_pk_fma_f32 v[66:67], v[66:67], s[36:37], v[6:7] op_sel_hi:[1,0,1]
	v_pk_fma_f32 v[68:69], v[68:69], s[36:37], v[2:3] op_sel_hi:[1,0,1]
	v_med3_f32 v76, v76, s70, v164
	v_med3_f32 v5, v77, s70, v164
	v_cvt_pk_fp8_f32 v75, v79, v65 op_sel:[0,0,1]
	v_pk_mul_f32 v[72:73], v[64:65], v[72:73] op_sel_hi:[0,1]
	v_pk_mul_f32 v[70:71], v[64:65], v[70:71] op_sel_hi:[0,1]
	v_pk_mul_f32 v[68:69], v[64:65], v[68:69] op_sel_hi:[0,1]
	v_pk_mul_f32 v[64:65], v[64:65], v[66:67] op_sel_hi:[0,1]
	v_cvt_pk_fp8_f32 v74, v76, v5 op_sel:[0,0,1]
	v_med3_f32 v5, v70, s70, v164
	v_med3_f32 v66, v64, s70, v164
	v_med3_f32 v67, v71, s70, v164
	v_med3_f32 v70, v65, s70, v164
	v_cvt_pk_fp8_f32 v64, v5, v67
	v_cvt_pk_fp8_f32 v65, v66, v70
	v_or_b32_e32 v62, 48, v4
	ds_read_b128 v[58:61], v123
	v_ashrrev_i32_e32 v63, 31, v62
	v_lshl_add_u32 v62, v62, 10, v146
	v_med3_f32 v71, v72, s70, v164
	v_med3_f32 v68, v68, s70, v164
	v_med3_f32 v5, v73, s70, v164
	v_med3_f32 v66, v69, s70, v164
	v_cvt_pk_fp8_f32 v64, v71, v5 op_sel:[0,0,1]
	v_cvt_pk_fp8_f32 v65, v68, v66 op_sel:[0,0,1]
	s_add_u32 s86, s16, s6
	s_addc_u32 s87, s17, s7
	s_waitcnt lgkmcnt(0)
	global_store_dwordx4 v62, v[58:61], s[86:87]
	ds_write2_b64 v122, v[74:75], v[64:65] offset1:4
	v_mul_f32_e32 v64, 0x41000000, v166
	v_pk_fma_f32 v[54:55], v[54:55], s[36:37], v[158:159] op_sel_hi:[1,0,1]
	v_pk_fma_f32 v[50:51], v[50:51], s[36:37], v[154:155] op_sel_hi:[1,0,1]
	v_pk_mul_f32 v[54:55], v[64:65], v[54:55] op_sel_hi:[0,1]
	v_pk_mul_f32 v[50:51], v[64:65], v[50:51] op_sel_hi:[0,1]
	v_med3_f32 v5, v54, s70, v164
	v_med3_f32 v54, v50, s70, v164
	v_med3_f32 v55, v55, s70, v164
	v_cvt_pk_fp8_f32 v50, v5, v55
	v_pk_fma_f32 v[56:57], v[56:57], s[36:37], v[156:157] op_sel_hi:[1,0,1]
	v_pk_fma_f32 v[52:53], v[52:53], s[36:37], v[152:153] op_sel_hi:[1,0,1]
	v_pk_mul_f32 v[56:57], v[64:65], v[56:57] op_sel_hi:[0,1]
	v_pk_mul_f32 v[52:53], v[64:65], v[52:53] op_sel_hi:[0,1]
	v_med3_f32 v65, v51, s70, v164
	v_pk_fma_f32 v[46:47], v[46:47], s[36:37], v[150:151] op_sel_hi:[1,0,1]
	v_pk_fma_f32 v[42:43], v[42:43], s[36:37], v[6:7] op_sel_hi:[1,0,1]
	v_med3_f32 v56, v56, s70, v164
	v_med3_f32 v5, v57, s70, v164
	v_pk_mul_f32 v[46:47], v[64:65], v[46:47] op_sel_hi:[0,1]
	v_pk_mul_f32 v[42:43], v[64:65], v[42:43] op_sel_hi:[0,1]
	v_cvt_pk_fp8_f32 v50, v56, v5 op_sel:[0,0,1]
	v_med3_f32 v5, v46, s70, v164
	v_med3_f32 v46, v42, s70, v164
	v_med3_f32 v47, v47, s70, v164
	v_cvt_pk_fp8_f32 v42, v5, v47
	v_pk_fma_f32 v[48:49], v[48:49], s[36:37], v[8:9] op_sel_hi:[1,0,1]
	v_pk_mul_f32 v[48:49], v[64:65], v[48:49] op_sel_hi:[0,1]
	v_med3_f32 v48, v48, s70, v164
	v_med3_f32 v5, v49, s70, v164
	v_cvt_pk_fp8_f32 v42, v48, v5 op_sel:[0,0,1]
	v_mul_f32_e32 v48, 0x41000000, v165
	v_pk_fma_f32 v[38:39], v[38:39], s[36:37], v[158:159] op_sel_hi:[1,0,1]
	v_pk_fma_f32 v[34:35], v[34:35], s[36:37], v[154:155] op_sel_hi:[1,0,1]
	v_cvt_pk_fp8_f32 v51, v54, v65
	v_pk_mul_f32 v[38:39], v[48:49], v[38:39] op_sel_hi:[0,1]
	v_pk_mul_f32 v[34:35], v[48:49], v[34:35] op_sel_hi:[0,1]
	v_med3_f32 v5, v38, s70, v164
	v_med3_f32 v38, v34, s70, v164
	v_med3_f32 v39, v39, s70, v164
	v_cvt_pk_fp8_f32 v34, v5, v39
	v_med3_f32 v52, v52, s70, v164
	v_med3_f32 v53, v53, s70, v164
	v_pk_fma_f32 v[40:41], v[40:41], s[36:37], v[156:157] op_sel_hi:[1,0,1]
	v_pk_fma_f32 v[36:37], v[36:37], s[36:37], v[152:153] op_sel_hi:[1,0,1]
	v_cvt_pk_fp8_f32 v51, v52, v53 op_sel:[0,0,1]
	v_med3_f32 v52, v43, s70, v164
	v_pk_mul_f32 v[40:41], v[48:49], v[40:41] op_sel_hi:[0,1]
	v_pk_mul_f32 v[36:37], v[48:49], v[36:37] op_sel_hi:[0,1]
	v_med3_f32 v49, v35, s70, v164
	v_pk_fma_f32 v[30:31], v[30:31], s[36:37], v[150:151] op_sel_hi:[1,0,1]
	v_pk_fma_f32 v[26:27], v[26:27], s[36:37], v[6:7] op_sel_hi:[1,0,1]
	v_cvt_pk_fp8_f32 v43, v46, v52
	v_med3_f32 v40, v40, s70, v164
	v_med3_f32 v5, v41, s70, v164
	v_pk_mul_f32 v[30:31], v[48:49], v[30:31] op_sel_hi:[0,1]
	v_pk_mul_f32 v[26:27], v[48:49], v[26:27] op_sel_hi:[0,1]
	v_add_u32_e32 v62, 0x80, v4
	v_pk_fma_f32 v[44:45], v[44:45], s[36:37], v[2:3] op_sel_hi:[1,0,1]
	v_cvt_pk_fp8_f32 v34, v40, v5 op_sel:[0,0,1]
	v_med3_f32 v5, v30, s70, v164
	v_med3_f32 v30, v26, s70, v164
	v_med3_f32 v31, v31, s70, v164
	ds_read_b128 v[58:61], v123
	v_ashrrev_i32_e32 v63, 31, v62
	v_pk_mul_f32 v[44:45], v[64:65], v[44:45] op_sel_hi:[0,1]
	v_cvt_pk_fp8_f32 v35, v38, v49
	v_cvt_pk_fp8_f32 v26, v5, v31
	v_lshl_add_u32 v62, v62, 10, v146
	v_med3_f32 v44, v44, s70, v164
	v_med3_f32 v45, v45, s70, v164
	v_pk_fma_f32 v[32:33], v[32:33], s[36:37], v[8:9] op_sel_hi:[1,0,1]
	v_cvt_pk_fp8_f32 v43, v44, v45 op_sel:[0,0,1]
	v_pk_mul_f32 v[32:33], v[48:49], v[32:33] op_sel_hi:[0,1]
	s_add_u32 s86, s16, s6
	s_addc_u32 s87, s17, s7
	v_med3_f32 v36, v36, s70, v164
	v_med3_f32 v37, v37, s70, v164
	v_med3_f32 v32, v32, s70, v164
	v_med3_f32 v5, v33, s70, v164
	v_mov_b32_e32 v44, v62
	v_cvt_pk_fp8_f32 v35, v36, v37 op_sel:[0,0,1]
	v_med3_f32 v36, v27, s70, v164
	v_cvt_pk_fp8_f32 v26, v32, v5 op_sel:[0,0,1]
	v_mul_f32_e32 v32, 0x41000000, v1
	v_pk_fma_f32 v[22:23], v[22:23], s[36:37], v[158:159] op_sel_hi:[1,0,1]
	v_pk_fma_f32 v[18:19], v[18:19], s[36:37], v[154:155] op_sel_hi:[1,0,1]
	s_waitcnt lgkmcnt(0)
	global_store_dwordx4 v44, v[58:61], s[86:87]
	v_cvt_pk_fp8_f32 v27, v30, v36
	v_pk_mul_f32 v[22:23], v[32:33], v[22:23] op_sel_hi:[0,1]
	v_pk_mul_f32 v[18:19], v[32:33], v[18:19] op_sel_hi:[0,1]
	ds_write2_b64 v122, v[50:51], v[42:43] offset1:4
	v_add_u32_e32 v46, 0x90, v4
	v_pk_fma_f32 v[28:29], v[28:29], s[36:37], v[2:3] op_sel_hi:[1,0,1]
	v_med3_f32 v1, v22, s70, v164
	v_med3_f32 v5, v18, s70, v164
	v_med3_f32 v22, v23, s70, v164
	v_med3_f32 v23, v19, s70, v164
	ds_read_b128 v[42:45], v123
	v_ashrrev_i32_e32 v47, 31, v46
	v_pk_mul_f32 v[28:29], v[48:49], v[28:29] op_sel_hi:[0,1]
	v_cvt_pk_fp8_f32 v18, v1, v22
	v_cvt_pk_fp8_f32 v19, v5, v23
	v_lshl_add_u32 v46, v46, 10, v146
	v_med3_f32 v28, v28, s70, v164
	v_med3_f32 v29, v29, s70, v164
	v_pk_fma_f32 v[24:25], v[24:25], s[36:37], v[156:157] op_sel_hi:[1,0,1]
	v_pk_fma_f32 v[20:21], v[20:21], s[36:37], v[152:153] op_sel_hi:[1,0,1]
	v_cvt_pk_fp8_f32 v27, v28, v29 op_sel:[0,0,1]
	v_pk_mul_f32 v[24:25], v[32:33], v[24:25] op_sel_hi:[0,1]
	v_pk_mul_f32 v[20:21], v[32:33], v[20:21] op_sel_hi:[0,1]
	v_pk_fma_f32 v[14:15], v[14:15], s[36:37], v[150:151] op_sel_hi:[1,0,1]
	v_pk_fma_f32 v[6:7], v[10:11], s[36:37], v[6:7] op_sel_hi:[1,0,1]
	s_add_u32 s86, s16, s6
	s_addc_u32 s87, s17, s7
	v_med3_f32 v24, v24, s70, v164
	v_med3_f32 v20, v20, s70, v164
	v_med3_f32 v1, v25, s70, v164
	v_med3_f32 v5, v21, s70, v164
	v_pk_mul_f32 v[14:15], v[32:33], v[14:15] op_sel_hi:[0,1]
	v_pk_mul_f32 v[6:7], v[32:33], v[6:7] op_sel_hi:[0,1]
	v_mov_b32_e32 v28, v46
	v_cvt_pk_fp8_f32 v18, v24, v1 op_sel:[0,0,1]
	v_cvt_pk_fp8_f32 v19, v20, v5 op_sel:[0,0,1]
	v_med3_f32 v1, v14, s70, v164
	v_med3_f32 v5, v6, s70, v164
	v_med3_f32 v10, v15, s70, v164
	v_med3_f32 v11, v7, s70, v164
	s_waitcnt lgkmcnt(0)
	global_store_dwordx4 v28, v[42:45], s[86:87]
	v_cvt_pk_fp8_f32 v6, v1, v10
	v_cvt_pk_fp8_f32 v7, v5, v11
	ds_write2_b64 v122, v[34:35], v[26:27] offset1:4
	v_add_u32_e32 v30, 0xa0, v4
	v_pk_fma_f32 v[8:9], v[16:17], s[36:37], v[8:9] op_sel_hi:[1,0,1]
	v_pk_fma_f32 v[2:3], v[12:13], s[36:37], v[2:3] op_sel_hi:[1,0,1]
	ds_read_b128 v[26:29], v123
	v_ashrrev_i32_e32 v31, 31, v30
	v_pk_mul_f32 v[8:9], v[32:33], v[8:9] op_sel_hi:[0,1]
	v_pk_mul_f32 v[2:3], v[32:33], v[2:3] op_sel_hi:[0,1]
	v_lshl_add_u32 v30, v30, 10, v146
	v_med3_f32 v8, v8, s70, v164
	v_med3_f32 v2, v2, s70, v164
	v_med3_f32 v1, v9, s70, v164
	v_med3_f32 v3, v3, s70, v164
	v_cvt_pk_fp8_f32 v6, v8, v1 op_sel:[0,0,1]
	v_cvt_pk_fp8_f32 v7, v2, v3 op_sel:[0,0,1]
	s_add_u32 s86, s16, s6
	s_addc_u32 s87, s17, s7
	v_mov_b32_e32 v2, v30
	s_waitcnt lgkmcnt(0)
	global_store_dwordx4 v2, v[26:29], s[86:87]
	ds_write2_b64 v122, v[18:19], v[6:7] offset1:4
	v_add_u32_e32 v2, 0xb0, v4
	ds_read_b128 v[6:9], v123
	v_ashrrev_i32_e32 v3, 31, v2
	v_lshl_add_u32 v2, v2, 10, v146
	s_add_u32 s86, s16, s6
	s_addc_u32 s87, s17, s7
	s_waitcnt lgkmcnt(0)
	global_store_dwordx4 v2, v[6:9], s[86:87]
	s_and_b64 vcc, exec, s[8:9]
	s_mov_b64 s[6:7], -1
	s_cbranch_vccnz .LBB0_1616
	v_mov_b32_e32 v12, v0
	s_lshl_b32 s7, s40, 8
	v_readfirstlane_b32 s6, v12
	s_and_b32 s8, s6, 0xc0
	s_ashr_i32 s6, s6, 2
	s_andn2_b32 s6, s6, 63
	s_add_i32 s6, s6, s7
	v_and_or_b32 v2, v12, 15, s6
	v_lshlrev_b32_e32 v4, 2, v2
	s_lshl_b64 s[6:7], s[42:43], 11
	s_add_u32 s9, s56, s6
	s_addc_u32 s39, s57, s7
	s_lshl_b32 s6, s38, 8
	global_load_dword v146, v4, s[12:13] offset:0
	global_load_dword v170, v4, s[12:13] offset:64
	global_load_dword v169, v4, s[12:13] offset:128
	global_load_dword v168, v4, s[12:13] offset:192
	global_load_dword v167, v4, s[12:13] offset:512
	global_load_dword v166, v4, s[12:13] offset:576
	global_load_dword v165, v4, s[12:13] offset:640
	global_load_dword v1, v4, s[12:13] offset:704
	s_ashr_i32 s7, s6, 31
	s_lshl_b64 s[6:7], s[6:7], 1
	s_add_u32 s6, s9, s6
	s_addc_u32 s7, s39, s7
	s_lshl_b32 s8, s8, 1
	s_add_u32 s6, s6, s8
	s_addc_u32 s7, s7, 0
	v_and_b32_e32 v2, 48, v12
	global_load_dwordx4 v[6:9], v2, s[6:7]
	s_nop 0
	global_load_dwordx4 v[2:5], v2, s[6:7] offset:64
	s_andn2_b64 vcc, exec, s[14:15]
	s_cbranch_vccnz .LBB0_1615
	s_barrier
	s_branch .LBB0_1615

.LBB0_3348:
	s_mov_b32 s82, 0xc2700000
	v_mov_b32_e32 v190, 0x41898193
	v_lshlrev_b32_e32 v160, 16, v46
	v_and_b32_e32 v161, 0xffff0000, v46
	v_lshlrev_b32_e32 v156, 16, v42
	v_and_b32_e32 v157, 0xffff0000, v42
	v_mul_f32_e32 v42, 0x3d800000, v179
	v_lshlrev_b32_e32 v154, 16, v47
	v_and_b32_e32 v155, 0xffff0000, v47
	v_lshlrev_b32_e32 v46, 16, v44
	v_and_b32_e32 v47, 0xffff0000, v44
	v_lshlrev_b32_e32 v150, 16, v45
	v_and_b32_e32 v151, 0xffff0000, v45
	v_pk_fma_f32 v[44:45], v[42:43], v[130:131], v[160:161] op_sel_hi:[0,1,1]
	v_med3_f32 v44, v44, s82, v190
	v_med3_f32 v45, v45, s82, v190
	v_exp_f32_e64 v130, -v44
	v_exp_f32_e64 v131, -v45
	v_pk_fma_f32 v[132:133], v[42:43], v[132:133], v[154:155] op_sel_hi:[0,1,1]
	v_med3_f32 v132, v132, s82, v190
	v_med3_f32 v133, v133, s82, v190
	v_pk_add_f32 v[130:131], v[130:131], 1.0 op_sel_hi:[1,0]
	v_exp_f32_e64 v188, -v132
	v_exp_f32_e64 v189, -v133
	v_lshlrev_b32_e32 v152, 16, v48
	v_and_b32_e32 v153, 0xffff0000, v48
	v_pk_add_f32 v[188:189], v[188:189], 1.0 op_sel_hi:[1,0]
	v_pk_fma_f32 v[122:123], v[42:43], v[122:123], v[152:153] op_sel_hi:[0,1,1]
	v_pk_mul_f32 v[184:185], v[130:131], v[188:189]
	v_rcp_f32_e32 v184, v184
	v_rcp_f32_e32 v185, v185
	s_nop 0
	v_pk_mul_f32 v[186:187], v[184:185], v[188:189]
	v_pk_mul_f32 v[188:189], v[184:185], v[130:131]
	v_pk_mul_f32 v[44:45], v[44:45], v[186:187]
	v_med3_f32 v122, v122, s82, v190
	v_med3_f32 v123, v123, s82, v190
	v_lshlrev_b32_e32 v48, 16, v49
	v_pk_mul_f32 v[130:131], v[132:133], v[188:189]
	v_exp_f32_e64 v132, -v122
	v_exp_f32_e64 v133, -v123
	v_and_b32_e32 v49, 0xffff0000, v49
	v_pk_fma_f32 v[124:125], v[42:43], v[124:125], v[48:49] op_sel_hi:[0,1,1]
	v_lshlrev_b32_e32 v158, 16, v43
	v_and_b32_e32 v159, 0xffff0000, v43
	v_med3_f32 v124, v124, s82, v190
	v_med3_f32 v125, v125, s82, v190
	v_pk_fma_f32 v[136:137], v[42:43], v[136:137], v[158:159] op_sel_hi:[0,1,1]
	v_pk_fma_f32 v[134:135], v[42:43], v[134:135], v[156:157] op_sel_hi:[0,1,1]
	v_pk_fma_f32 v[128:129], v[42:43], v[128:129], v[150:151] op_sel_hi:[0,1,1]
	v_pk_add_f32 v[132:133], v[132:133], 1.0 op_sel_hi:[1,0]
	v_pk_fma_f32 v[42:43], v[42:43], v[126:127], v[46:47] op_sel_hi:[0,1,1]
	v_exp_f32_e64 v188, -v124
	v_exp_f32_e64 v189, -v125
	v_med3_f32 v42, v42, s81, v170
	v_pk_add_f32 v[188:189], v[188:189], 1.0 op_sel_hi:[1,0]
	v_med3_f32 v43, v43, s81, v170
	v_pk_mul_f32 v[184:185], v[132:133], v[188:189]
	v_rcp_f32_e32 v184, v184
	v_rcp_f32_e32 v185, v185
	s_nop 0
	v_pk_mul_f32 v[186:187], v[184:185], v[188:189]
	v_pk_mul_f32 v[188:189], v[184:185], v[132:133]
	v_pk_mul_f32 v[122:123], v[122:123], v[186:187]
	v_pk_mul_f32 v[42:43], v[122:123], v[42:43]
	v_med3_f32 v123, v129, s81, v170
	v_cvt_pk_fp8_f32 v129, v42, v43
	v_med3_f32 v122, v128, s81, v170
	v_pk_mul_f32 v[42:43], v[124:125], v[188:189]
	v_med3_f32 v134, v134, s81, v170
	v_med3_f32 v135, v135, s81, v170
	v_pk_mul_f32 v[42:43], v[42:43], v[122:123]
	v_pk_mul_f32 v[44:45], v[44:45], v[134:135]
	v_cvt_pk_fp8_f32 v129, v42, v43 op_sel:[0,0,1]
	v_mul_f32_e32 v42, 0x3d800000, v178
	v_cvt_pk_fp8_f32 v128, v44, v45
	v_pk_fma_f32 v[44:45], v[42:43], v[114:115], v[160:161] op_sel_hi:[0,1,1]
	v_med3_f32 v44, v44, s82, v190
	v_med3_f32 v45, v45, s82, v190
	v_exp_f32_e64 v114, -v44
	v_exp_f32_e64 v115, -v45
	v_pk_fma_f32 v[116:117], v[42:43], v[116:117], v[154:155] op_sel_hi:[0,1,1]
	v_med3_f32 v116, v116, s82, v190
	v_med3_f32 v117, v117, s82, v190
	v_pk_add_f32 v[114:115], v[114:115], 1.0 op_sel_hi:[1,0]
	v_exp_f32_e64 v188, -v116
	v_exp_f32_e64 v189, -v117
	v_pk_fma_f32 v[106:107], v[42:43], v[106:107], v[152:153] op_sel_hi:[0,1,1]
	v_med3_f32 v106, v106, s82, v190
	v_pk_add_f32 v[188:189], v[188:189], 1.0 op_sel_hi:[1,0]
	v_med3_f32 v107, v107, s82, v190
	v_pk_mul_f32 v[184:185], v[114:115], v[188:189]
	v_rcp_f32_e32 v184, v184
	v_rcp_f32_e32 v185, v185
	s_nop 0
	v_pk_mul_f32 v[186:187], v[184:185], v[188:189]
	v_pk_mul_f32 v[188:189], v[184:185], v[114:115]
	v_pk_mul_f32 v[44:45], v[44:45], v[186:187]
	v_pk_fma_f32 v[108:109], v[42:43], v[108:109], v[48:49] op_sel_hi:[0,1,1]
	v_med3_f32 v108, v108, s82, v190
	v_med3_f32 v109, v109, s82, v190
	v_pk_mul_f32 v[114:115], v[116:117], v[188:189]
	v_exp_f32_e64 v116, -v106
	v_exp_f32_e64 v117, -v107
	v_pk_fma_f32 v[120:121], v[42:43], v[120:121], v[158:159] op_sel_hi:[0,1,1]
	v_pk_fma_f32 v[118:119], v[42:43], v[118:119], v[156:157] op_sel_hi:[0,1,1]
	v_pk_fma_f32 v[112:113], v[42:43], v[112:113], v[150:151] op_sel_hi:[0,1,1]
	v_pk_add_f32 v[116:117], v[116:117], 1.0 op_sel_hi:[1,0]
	v_pk_fma_f32 v[42:43], v[42:43], v[110:111], v[46:47] op_sel_hi:[0,1,1]
	v_exp_f32_e64 v188, -v108
	v_exp_f32_e64 v189, -v109
	v_med3_f32 v118, v118, s81, v170
	v_pk_add_f32 v[188:189], v[188:189], 1.0 op_sel_hi:[1,0]
	v_med3_f32 v119, v119, s81, v170
	v_med3_f32 v42, v42, s81, v170
	v_med3_f32 v43, v43, s81, v170
	v_pk_mul_f32 v[184:185], v[116:117], v[188:189]
	v_rcp_f32_e32 v184, v184
	v_rcp_f32_e32 v185, v185
	s_nop 0
	v_pk_mul_f32 v[186:187], v[184:185], v[188:189]
	v_pk_mul_f32 v[188:189], v[184:185], v[116:117]
	v_pk_mul_f32 v[106:107], v[106:107], v[186:187]
	v_pk_mul_f32 v[44:45], v[44:45], v[118:119]
	v_pk_mul_f32 v[42:43], v[106:107], v[42:43]
	v_med3_f32 v106, v112, s81, v170
	v_med3_f32 v107, v113, s81, v170
	v_mov_b32_e32 v142, v0
	v_cvt_pk_fp8_f32 v112, v44, v45
	v_cvt_pk_fp8_f32 v113, v42, v43
	v_med3_f32 v134, v136, s81, v170
	v_readfirstlane_b32 s65, v142
	v_med3_f32 v135, v137, s81, v170
	s_ashr_i32 s10, s65, 6
	v_pk_mul_f32 v[130:131], v[130:131], v[134:135]
	v_med3_f32 v118, v120, s81, v170
	v_med3_f32 v119, v121, s81, v170
	v_pk_mul_f32 v[42:43], v[108:109], v[188:189]
	s_mul_i32 s11, s10, 0xb00
	v_cvt_pk_fp8_f32 v128, v130, v131 op_sel:[0,0,1]
	v_pk_mul_f32 v[114:115], v[114:115], v[118:119]
	v_pk_mul_f32 v[42:43], v[42:43], v[106:107]
	s_add_i32 s67, s11, 0
	v_and_b32_e32 v147, 15, v142
	v_lshrrev_b32_e32 v125, 1, v142
	v_cvt_pk_fp8_f32 v112, v114, v115 op_sel:[0,0,1]
	v_cvt_pk_fp8_f32 v113, v42, v43 op_sel:[0,0,1]
	s_add_i32 s67, s67, 0x20000
	v_mul_u32_u24_e32 v124, 48, v147
	v_and_b32_e32 v42, 24, v125
	v_add3_u32 v108, s67, v124, v42
	ds_write_b64 v108, v[128:129]
	ds_write_b64 v108, v[112:113] offset:768
	v_mul_f32_e32 v112, 0x3d800000, v177
	v_pk_fma_f32 v[98:99], v[112:113], v[98:99], v[160:161] op_sel_hi:[0,1,1]
	v_med3_f32 v98, v98, s82, v190
	v_med3_f32 v99, v99, s82, v190
	v_exp_f32_e64 v114, -v98
	v_exp_f32_e64 v115, -v99
	v_pk_fma_f32 v[100:101], v[112:113], v[100:101], v[154:155] op_sel_hi:[0,1,1]
	v_med3_f32 v100, v100, s82, v190
	v_med3_f32 v101, v101, s82, v190
	v_pk_add_f32 v[114:115], v[114:115], 1.0 op_sel_hi:[1,0]
	v_exp_f32_e64 v188, -v100
	v_exp_f32_e64 v189, -v101
	v_pk_fma_f32 v[102:103], v[112:113], v[102:103], v[156:157] op_sel_hi:[0,1,1]
	v_pk_fma_f32 v[90:91], v[112:113], v[90:91], v[152:153] op_sel_hi:[0,1,1]
	v_pk_add_f32 v[188:189], v[188:189], 1.0 op_sel_hi:[1,0]
	v_pk_fma_f32 v[104:105], v[112:113], v[104:105], v[158:159] op_sel_hi:[0,1,1]
	v_med3_f32 v102, v102, s81, v170
	v_med3_f32 v103, v103, s81, v170
	v_pk_mul_f32 v[184:185], v[114:115], v[188:189]
	v_rcp_f32_e32 v184, v184
	v_rcp_f32_e32 v185, v185
	s_nop 0
	v_pk_mul_f32 v[186:187], v[184:185], v[188:189]
	v_pk_mul_f32 v[188:189], v[184:185], v[114:115]
	v_pk_mul_f32 v[98:99], v[98:99], v[186:187]
	v_med3_f32 v90, v90, s82, v190
	v_med3_f32 v91, v91, s82, v190
	v_pk_mul_f32 v[98:99], v[98:99], v[102:103]
	v_med3_f32 v102, v104, s81, v170
	v_med3_f32 v103, v105, s81, v170
	v_exp_f32_e64 v104, -v90
	v_exp_f32_e64 v105, -v91
	v_pk_mul_f32 v[100:101], v[100:101], v[188:189]
	v_pk_fma_f32 v[92:93], v[112:113], v[92:93], v[48:49] op_sel_hi:[0,1,1]
	v_pk_mul_f32 v[100:101], v[100:101], v[102:103]
	v_pk_add_f32 v[102:103], v[104:105], 1.0 op_sel_hi:[1,0]
	v_med3_f32 v92, v92, s82, v190
	v_rcp_f32_e32 v102, v102
	v_rcp_f32_e32 v103, v103
	v_med3_f32 v93, v93, s82, v190
	v_pk_fma_f32 v[94:95], v[112:113], v[94:95], v[46:47] op_sel_hi:[0,1,1]
	v_pk_fma_f32 v[96:97], v[112:113], v[96:97], v[150:151] op_sel_hi:[0,1,1]
	v_pk_mul_f32 v[90:91], v[90:91], v[102:103]
	v_exp_f32_e64 v102, -v92
	v_exp_f32_e64 v103, -v93
	v_med3_f32 v94, v94, s81, v170
	v_med3_f32 v95, v95, s81, v170
	v_pk_mul_f32 v[90:91], v[90:91], v[94:95]
	v_med3_f32 v94, v96, s81, v170
	v_med3_f32 v95, v97, s81, v170
	v_pk_add_f32 v[96:97], v[102:103], 1.0 op_sel_hi:[1,0]
	v_rcp_f32_e32 v96, v96
	v_rcp_f32_e32 v97, v97
	v_cvt_pk_fp8_f32 v103, v90, v91
	v_bfe_u32 v106, v142, 1, 5
	v_pk_mul_f32 v[90:91], v[92:93], v[96:97]
	v_lshlrev_b32_e32 v43, 4, v142
	v_pk_mul_f32 v[90:91], v[90:91], v[94:95]
	s_ashr_i32 s65, s65, 2
	v_cvt_pk_fp8_f32 v103, v90, v91 op_sel:[0,0,1]
	v_mul_f32_e32 v90, 0x3d800000, v176
	v_pk_fma_f32 v[82:83], v[90:91], v[82:83], v[160:161] op_sel_hi:[0,1,1]
	v_med3_f32 v82, v82, s82, v190
	v_med3_f32 v83, v83, s82, v190
	v_exp_f32_e64 v92, -v82
	v_exp_f32_e64 v93, -v83
	v_pk_fma_f32 v[84:85], v[90:91], v[84:85], v[154:155] op_sel_hi:[0,1,1]
	v_med3_f32 v84, v84, s82, v190
	v_med3_f32 v85, v85, s82, v190
	v_pk_add_f32 v[92:93], v[92:93], 1.0 op_sel_hi:[1,0]
	v_exp_f32_e64 v188, -v84
	v_exp_f32_e64 v189, -v85
	v_pk_fma_f32 v[86:87], v[90:91], v[86:87], v[156:157] op_sel_hi:[0,1,1]
	v_pk_fma_f32 v[66:67], v[90:91], v[66:67], v[152:153] op_sel_hi:[0,1,1]
	v_pk_add_f32 v[188:189], v[188:189], 1.0 op_sel_hi:[1,0]
	v_pk_fma_f32 v[88:89], v[90:91], v[88:89], v[158:159] op_sel_hi:[0,1,1]
	v_med3_f32 v86, v86, s81, v170
	v_med3_f32 v87, v87, s81, v170
	v_pk_mul_f32 v[184:185], v[92:93], v[188:189]
	v_rcp_f32_e32 v184, v184
	v_rcp_f32_e32 v185, v185
	s_nop 0
	v_pk_mul_f32 v[186:187], v[184:185], v[188:189]
	v_pk_mul_f32 v[188:189], v[184:185], v[92:93]
	v_pk_mul_f32 v[82:83], v[82:83], v[186:187]
	v_med3_f32 v66, v66, s82, v190
	v_med3_f32 v67, v67, s82, v190
	v_pk_mul_f32 v[82:83], v[82:83], v[86:87]
	v_med3_f32 v86, v88, s81, v170
	v_med3_f32 v87, v89, s81, v170
	v_exp_f32_e64 v88, -v66
	v_exp_f32_e64 v89, -v67
	v_pk_mul_f32 v[84:85], v[84:85], v[188:189]
	v_pk_fma_f32 v[68:69], v[90:91], v[68:69], v[48:49] op_sel_hi:[0,1,1]
	v_pk_mul_f32 v[84:85], v[84:85], v[86:87]
	v_pk_add_f32 v[86:87], v[88:89], 1.0 op_sel_hi:[1,0]
	v_med3_f32 v68, v68, s82, v190
	v_rcp_f32_e32 v86, v86
	v_rcp_f32_e32 v87, v87
	v_med3_f32 v69, v69, s82, v190
	v_pk_fma_f32 v[74:75], v[90:91], v[74:75], v[46:47] op_sel_hi:[0,1,1]
	v_pk_fma_f32 v[76:77], v[90:91], v[76:77], v[150:151] op_sel_hi:[0,1,1]
	v_pk_mul_f32 v[66:67], v[66:67], v[86:87]
	v_exp_f32_e64 v86, -v68
	v_exp_f32_e64 v87, -v69
	v_med3_f32 v74, v74, s81, v170
	v_med3_f32 v75, v75, s81, v170
	v_pk_mul_f32 v[66:67], v[66:67], v[74:75]
	v_med3_f32 v74, v76, s81, v170
	v_med3_f32 v75, v77, s81, v170
	v_pk_add_f32 v[76:77], v[86:87], 1.0 op_sel_hi:[1,0]
	v_rcp_f32_e32 v76, v76
	v_rcp_f32_e32 v77, v77
	v_cvt_pk_fp8_f32 v87, v66, v67
	v_cvt_pk_fp8_f32 v102, v98, v99
	v_pk_mul_f32 v[66:67], v[68:69], v[76:77]
	v_mul_f32_e32 v68, 0x3d800000, v175
	v_pk_fma_f32 v[70:71], v[68:69], v[70:71], v[160:161] op_sel_hi:[0,1,1]
	v_med3_f32 v70, v70, s82, v190
	v_med3_f32 v71, v71, s82, v190
	v_pk_mul_f32 v[66:67], v[66:67], v[74:75]
	v_exp_f32_e64 v74, -v70
	v_exp_f32_e64 v75, -v71
	v_pk_fma_f32 v[72:73], v[68:69], v[72:73], v[154:155] op_sel_hi:[0,1,1]
	v_med3_f32 v72, v72, s82, v190
	v_med3_f32 v73, v73, s82, v190
	v_pk_add_f32 v[74:75], v[74:75], 1.0 op_sel_hi:[1,0]
	v_pk_fma_f32 v[76:77], v[68:69], v[80:81], v[158:159] op_sel_hi:[0,1,1]
	v_exp_f32_e64 v188, -v72
	v_exp_f32_e64 v189, -v73
	v_pk_fma_f32 v[58:59], v[68:69], v[58:59], v[152:153] op_sel_hi:[0,1,1]
	v_med3_f32 v58, v58, s82, v190
	v_pk_add_f32 v[188:189], v[188:189], 1.0 op_sel_hi:[1,0]
	v_med3_f32 v59, v59, s82, v190
	v_pk_mul_f32 v[184:185], v[74:75], v[188:189]
	v_rcp_f32_e32 v184, v184
	v_rcp_f32_e32 v185, v185
	s_nop 0
	v_pk_mul_f32 v[186:187], v[184:185], v[188:189]
	v_pk_mul_f32 v[188:189], v[184:185], v[74:75]
	v_pk_mul_f32 v[70:71], v[70:71], v[186:187]
	v_pk_fma_f32 v[60:61], v[68:69], v[60:61], v[48:49] op_sel_hi:[0,1,1]
	v_med3_f32 v60, v60, s82, v190
	v_med3_f32 v61, v61, s82, v190
	v_pk_mul_f32 v[72:73], v[72:73], v[188:189]
	v_exp_f32_e64 v74, -v58
	v_exp_f32_e64 v75, -v59
	v_pk_fma_f32 v[78:79], v[68:69], v[78:79], v[156:157] op_sel_hi:[0,1,1]
	v_pk_fma_f32 v[64:65], v[68:69], v[64:65], v[150:151] op_sel_hi:[0,1,1]
	v_pk_fma_f32 v[62:63], v[68:69], v[62:63], v[46:47] op_sel_hi:[0,1,1]
	v_pk_add_f32 v[74:75], v[74:75], 1.0 op_sel_hi:[1,0]
	v_exp_f32_e64 v188, -v60
	v_exp_f32_e64 v189, -v61
	v_med3_f32 v62, v62, s81, v170
	v_med3_f32 v63, v63, s81, v170
	v_mul_u32_u24_e32 v42, 48, v106
	v_pk_mul_f32 v[58:59], v[58:59], v[62:63]
	v_med3_f32 v62, v64, s81, v170
	v_med3_f32 v63, v65, s81, v170
	v_pk_add_f32 v[188:189], v[188:189], 1.0 op_sel_hi:[1,0]
	v_pk_mul_f32 v[184:185], v[74:75], v[188:189]
	v_rcp_f32_e32 v184, v184
	v_rcp_f32_e32 v185, v185
	s_nop 0
	v_pk_mul_f32 v[186:187], v[184:185], v[188:189]
	v_pk_mul_f32 v[188:189], v[184:185], v[74:75]
	v_pk_mul_f32 v[58:59], v[58:59], v[186:187]
	v_cvt_pk_fp8_f32 v69, v58, v59
	v_and_b32_e32 v142, 16, v43
	s_andn2_b32 s65, s65, 63
	v_pk_mul_f32 v[58:59], v[60:61], v[188:189]
	v_lshl_or_b32 v106, s74, 8, v106
	v_pk_mul_f32 v[58:59], v[58:59], v[62:63]
	v_cvt_pk_fp8_f32 v86, v82, v83
	v_cvt_pk_fp8_f32 v69, v58, v59 op_sel:[0,0,1]
	v_mul_f32_e32 v58, 0x3d800000, v174
	v_pk_fma_f32 v[50:51], v[58:59], v[50:51], v[160:161] op_sel_hi:[0,1,1]
	v_med3_f32 v50, v50, s82, v190
	v_med3_f32 v51, v51, s82, v190
	v_exp_f32_e64 v60, -v50
	v_exp_f32_e64 v61, -v51
	v_pk_fma_f32 v[52:53], v[58:59], v[52:53], v[154:155] op_sel_hi:[0,1,1]
	v_med3_f32 v52, v52, s82, v190
	v_med3_f32 v53, v53, s82, v190
	v_pk_add_f32 v[60:61], v[60:61], 1.0 op_sel_hi:[1,0]
	v_exp_f32_e64 v188, -v52
	v_exp_f32_e64 v189, -v53
	v_pk_fma_f32 v[54:55], v[58:59], v[54:55], v[156:157] op_sel_hi:[0,1,1]
	v_pk_fma_f32 v[34:35], v[58:59], v[34:35], v[152:153] op_sel_hi:[0,1,1]
	v_pk_add_f32 v[188:189], v[188:189], 1.0 op_sel_hi:[1,0]
	v_pk_fma_f32 v[56:57], v[58:59], v[56:57], v[158:159] op_sel_hi:[0,1,1]
	v_med3_f32 v54, v54, s81, v170
	v_med3_f32 v55, v55, s81, v170
	v_pk_mul_f32 v[184:185], v[60:61], v[188:189]
	v_rcp_f32_e32 v184, v184
	v_rcp_f32_e32 v185, v185
	s_nop 0
	v_pk_mul_f32 v[186:187], v[184:185], v[188:189]
	v_pk_mul_f32 v[188:189], v[184:185], v[60:61]
	v_pk_mul_f32 v[50:51], v[50:51], v[186:187]
	v_med3_f32 v34, v34, s82, v190
	v_med3_f32 v35, v35, s82, v190
	v_pk_mul_f32 v[50:51], v[50:51], v[54:55]
	v_med3_f32 v54, v56, s81, v170
	v_med3_f32 v55, v57, s81, v170
	v_exp_f32_e64 v56, -v34
	v_exp_f32_e64 v57, -v35
	v_pk_mul_f32 v[52:53], v[52:53], v[188:189]
	v_pk_fma_f32 v[36:37], v[58:59], v[36:37], v[48:49] op_sel_hi:[0,1,1]
	v_pk_mul_f32 v[52:53], v[52:53], v[54:55]
	v_pk_add_f32 v[54:55], v[56:57], 1.0 op_sel_hi:[1,0]
	v_med3_f32 v36, v36, s82, v190
	v_med3_f32 v37, v37, s82, v190
	s_lshl_b32 s10, s10, 5
	v_add3_u32 v109, s67, v42, v142
	v_add_u32_e32 v106, s65, v106
	v_exp_f32_e64 v188, -v36
	v_exp_f32_e64 v189, -v37
	s_lshl_b32 s11, s76, 7
	s_and_b32 s10, s10, 0x60
	ds_read_b128 v[42:45], v109
	v_ashrrev_i32_e32 v107, 31, v106
	s_or_b32 s10, s10, s11
	v_lshl_add_u32 v110, v106, 10, v142
	v_cvt_pk_fp8_f32 v102, v100, v101 op_sel:[0,0,1]
	v_pk_fma_f32 v[38:39], v[58:59], v[38:39], v[46:47] op_sel_hi:[0,1,1]
	s_ashr_i32 s11, s10, 31
	v_cvt_pk_fp8_f32 v86, v84, v85 op_sel:[0,0,1]
	v_cvt_pk_fp8_f32 v87, v66, v67 op_sel:[0,0,1]
	v_pk_fma_f32 v[40:41], v[58:59], v[40:41], v[150:151] op_sel_hi:[0,1,1]
	v_med3_f32 v38, v38, s81, v170
	v_med3_f32 v39, v39, s81, v170
	s_add_u32 s86, s18, s10
	s_addc_u32 s87, s19, s11
	v_pk_mul_f32 v[34:35], v[34:35], v[38:39]
	v_med3_f32 v38, v40, s81, v170
	v_med3_f32 v39, v41, s81, v170
	v_pk_add_f32 v[188:189], v[188:189], 1.0 op_sel_hi:[1,0]
	v_mov_b32_e32 v66, v110
	v_pk_mul_f32 v[184:185], v[54:55], v[188:189]
	v_rcp_f32_e32 v184, v184
	v_rcp_f32_e32 v185, v185
	s_nop 0
	v_pk_mul_f32 v[186:187], v[184:185], v[188:189]
	v_pk_mul_f32 v[188:189], v[184:185], v[54:55]
	v_pk_mul_f32 v[34:35], v[34:35], v[186:187]
	s_waitcnt lgkmcnt(0)
	global_store_dwordx4 v66, v[42:45], s[86:87]
	ds_write_b64 v108, v[102:103]
	ds_write_b64 v108, v[86:87] offset:768
	v_or_b32_e32 v66, 32, v106
	ds_read_b128 v[42:45], v109
	v_ashrrev_i32_e32 v67, 31, v66
	v_cvt_pk_fp8_f32 v55, v34, v35
	v_lshl_add_u32 v66, v66, 10, v142
	v_pk_mul_f32 v[34:35], v[36:37], v[188:189]
	v_mul_f32_e32 v40, 0x3d800000, v171
	s_add_u32 s86, s18, s10
	s_addc_u32 s87, s19, s11
	v_pk_mul_f32 v[34:35], v[34:35], v[38:39]
	v_pk_fma_f32 v[26:27], v[40:41], v[26:27], v[160:161] op_sel_hi:[0,1,1]
	v_cvt_pk_fp8_f32 v55, v34, v35 op_sel:[0,0,1]
	v_mov_b32_e32 v34, v66
	v_med3_f32 v26, v26, s82, v190
	v_med3_f32 v27, v27, s82, v190
	s_waitcnt lgkmcnt(0)
	global_store_dwordx4 v34, v[42:45], s[86:87]
	v_pk_fma_f32 v[28:29], v[40:41], v[28:29], v[154:155] op_sel_hi:[0,1,1]
	v_med3_f32 v28, v28, s82, v190
	v_exp_f32_e64 v42, -v26
	v_exp_f32_e64 v43, -v27
	v_med3_f32 v29, v29, s82, v190
	v_exp_f32_e64 v188, -v28
	v_exp_f32_e64 v189, -v29
	v_pk_add_f32 v[42:43], v[42:43], 1.0 op_sel_hi:[1,0]
	v_pk_fma_f32 v[30:31], v[40:41], v[30:31], v[156:157] op_sel_hi:[0,1,1]
	v_pk_fma_f32 v[18:19], v[40:41], v[18:19], v[152:153] op_sel_hi:[0,1,1]
	v_pk_fma_f32 v[32:33], v[40:41], v[32:33], v[158:159] op_sel_hi:[0,1,1]
	v_med3_f32 v30, v30, s81, v170
	v_pk_add_f32 v[188:189], v[188:189], 1.0 op_sel_hi:[1,0]
	v_med3_f32 v31, v31, s81, v170
	v_pk_mul_f32 v[184:185], v[42:43], v[188:189]
	v_rcp_f32_e32 v184, v184
	v_rcp_f32_e32 v185, v185
	s_nop 0
	v_pk_mul_f32 v[186:187], v[184:185], v[188:189]
	v_pk_mul_f32 v[188:189], v[184:185], v[42:43]
	v_pk_mul_f32 v[26:27], v[26:27], v[186:187]
	v_med3_f32 v18, v18, s82, v190
	v_med3_f32 v19, v19, s82, v190
	v_pk_mul_f32 v[26:27], v[26:27], v[30:31]
	v_med3_f32 v30, v32, s81, v170
	v_med3_f32 v31, v33, s81, v170
	v_exp_f32_e64 v32, -v18
	v_exp_f32_e64 v33, -v19
	v_pk_mul_f32 v[28:29], v[28:29], v[188:189]
	v_pk_fma_f32 v[20:21], v[40:41], v[20:21], v[48:49] op_sel_hi:[0,1,1]
	v_pk_mul_f32 v[28:29], v[28:29], v[30:31]
	v_pk_add_f32 v[30:31], v[32:33], 1.0 op_sel_hi:[1,0]
	v_med3_f32 v20, v20, s82, v190
	v_rcp_f32_e32 v30, v30
	v_rcp_f32_e32 v31, v31
	v_med3_f32 v21, v21, s82, v190
	v_pk_fma_f32 v[22:23], v[40:41], v[22:23], v[46:47] op_sel_hi:[0,1,1]
	v_pk_fma_f32 v[24:25], v[40:41], v[24:25], v[150:151] op_sel_hi:[0,1,1]
	v_pk_mul_f32 v[18:19], v[18:19], v[30:31]
	v_exp_f32_e64 v30, -v20
	v_exp_f32_e64 v31, -v21
	v_med3_f32 v22, v22, s81, v170
	v_med3_f32 v23, v23, s81, v170
	v_pk_mul_f32 v[18:19], v[18:19], v[22:23]
	v_med3_f32 v22, v24, s81, v170
	v_med3_f32 v23, v25, s81, v170
	v_pk_add_f32 v[24:25], v[30:31], 1.0 op_sel_hi:[1,0]
	v_rcp_f32_e32 v24, v24
	v_rcp_f32_e32 v25, v25
	v_cvt_pk_fp8_f32 v31, v18, v19
	v_med3_f32 v78, v78, s81, v170
	v_med3_f32 v79, v79, s81, v170
	v_pk_mul_f32 v[18:19], v[20:21], v[24:25]
	v_pk_mul_f32 v[70:71], v[70:71], v[78:79]
	v_pk_mul_f32 v[18:19], v[18:19], v[22:23]
	v_cvt_pk_fp8_f32 v31, v18, v19 op_sel:[0,0,1]
	v_mul_f32_e32 v18, 0x3d800000, v169
	v_pk_fma_f32 v[10:11], v[18:19], v[10:11], v[160:161] op_sel_hi:[0,1,1]
	v_med3_f32 v10, v10, s82, v190
	v_med3_f32 v11, v11, s82, v190
	v_exp_f32_e64 v20, -v10
	v_exp_f32_e64 v21, -v11
	v_pk_fma_f32 v[12:13], v[18:19], v[12:13], v[154:155] op_sel_hi:[0,1,1]
	v_med3_f32 v12, v12, s82, v190
	v_med3_f32 v13, v13, s82, v190
	v_pk_add_f32 v[20:21], v[20:21], 1.0 op_sel_hi:[1,0]
	v_exp_f32_e64 v188, -v12
	v_exp_f32_e64 v189, -v13
	v_pk_fma_f32 v[14:15], v[18:19], v[14:15], v[156:157] op_sel_hi:[0,1,1]
	v_pk_fma_f32 v[2:3], v[18:19], v[2:3], v[152:153] op_sel_hi:[0,1,1]
	v_pk_add_f32 v[188:189], v[188:189], 1.0 op_sel_hi:[1,0]
	v_pk_fma_f32 v[16:17], v[18:19], v[16:17], v[158:159] op_sel_hi:[0,1,1]
	v_med3_f32 v14, v14, s81, v170
	v_med3_f32 v15, v15, s81, v170
	v_pk_mul_f32 v[184:185], v[20:21], v[188:189]
	v_rcp_f32_e32 v184, v184
	v_rcp_f32_e32 v185, v185
	s_nop 0
	v_pk_mul_f32 v[186:187], v[184:185], v[188:189]
	v_pk_mul_f32 v[188:189], v[184:185], v[20:21]
	v_pk_mul_f32 v[10:11], v[10:11], v[186:187]
	v_med3_f32 v2, v2, s82, v190
	v_med3_f32 v3, v3, s82, v190
	v_pk_mul_f32 v[10:11], v[10:11], v[14:15]
	v_med3_f32 v14, v16, s81, v170
	v_med3_f32 v15, v17, s81, v170
	v_exp_f32_e64 v16, -v2
	v_exp_f32_e64 v17, -v3
	v_pk_mul_f32 v[12:13], v[12:13], v[188:189]
	v_pk_fma_f32 v[4:5], v[18:19], v[4:5], v[48:49] op_sel_hi:[0,1,1]
	v_pk_mul_f32 v[12:13], v[12:13], v[14:15]
	v_pk_add_f32 v[14:15], v[16:17], 1.0 op_sel_hi:[1,0]
	v_med3_f32 v4, v4, s82, v190
	v_med3_f32 v5, v5, s82, v190
	v_cvt_pk_fp8_f32 v68, v70, v71
	v_exp_f32_e64 v188, -v4
	v_exp_f32_e64 v189, -v5
	v_cvt_pk_fp8_f32 v54, v50, v51
	v_med3_f32 v76, v76, s81, v170
	v_med3_f32 v77, v77, s81, v170
	v_pk_fma_f32 v[6:7], v[18:19], v[6:7], v[46:47] op_sel_hi:[0,1,1]
	v_pk_mul_f32 v[72:73], v[72:73], v[76:77]
	v_pk_fma_f32 v[8:9], v[18:19], v[8:9], v[150:151] op_sel_hi:[0,1,1]
	v_med3_f32 v6, v6, s81, v170
	v_med3_f32 v7, v7, s81, v170
	v_cvt_pk_fp8_f32 v68, v72, v73 op_sel:[0,0,1]
	v_pk_mul_f32 v[2:3], v[2:3], v[6:7]
	v_med3_f32 v6, v8, s81, v170
	v_med3_f32 v7, v9, s81, v170
	v_pk_add_f32 v[188:189], v[188:189], 1.0 op_sel_hi:[1,0]
	v_cvt_pk_fp8_f32 v54, v52, v53 op_sel:[0,0,1]
	v_pk_mul_f32 v[184:185], v[14:15], v[188:189]
	v_rcp_f32_e32 v184, v184
	v_rcp_f32_e32 v185, v185
	s_nop 0
	v_pk_mul_f32 v[186:187], v[184:185], v[188:189]
	v_pk_mul_f32 v[188:189], v[184:185], v[14:15]
	v_pk_mul_f32 v[2:3], v[2:3], v[186:187]
	v_cvt_pk_fp8_f32 v30, v26, v27
	v_cvt_pk_fp8_f32 v14, v10, v11
	v_cvt_pk_fp8_f32 v15, v2, v3
	ds_write_b64 v108, v[68:69]
	ds_write_b64 v108, v[54:55] offset:768
	v_add_u32_e32 v38, 0x80, v106
	ds_read_b128 v[34:37], v109
	v_ashrrev_i32_e32 v39, 31, v38
	v_pk_mul_f32 v[2:3], v[4:5], v[188:189]
	v_lshl_add_u32 v38, v38, 10, v142
	v_cvt_pk_fp8_f32 v30, v28, v29 op_sel:[0,0,1]
	v_pk_mul_f32 v[2:3], v[2:3], v[6:7]
	v_cvt_pk_fp8_f32 v14, v12, v13 op_sel:[0,0,1]
	v_cvt_pk_fp8_f32 v15, v2, v3 op_sel:[0,0,1]
	s_add_u32 s86, s18, s10
	s_addc_u32 s87, s19, s11
	v_mov_b32_e32 v2, v38
	s_waitcnt lgkmcnt(0)
	global_store_dwordx4 v2, v[34:37], s[86:87]
	ds_write_b64 v108, v[30:31]
	ds_write_b64 v108, v[14:15] offset:768
	v_add_u32_e32 v6, 0xa0, v106
	ds_read_b128 v[2:5], v109
	v_ashrrev_i32_e32 v7, 31, v6
	v_lshl_add_u32 v6, v6, 10, v142
	s_add_u32 s86, s18, s10
	s_addc_u32 s87, s19, s11
	s_and_b64 vcc, exec, s[8:9]
	s_mov_b64 s[8:9], -1
	s_waitcnt lgkmcnt(0)
	global_store_dwordx4 v6, v[2:5], s[86:87]
	s_cbranch_vccnz .LBB0_3339
	s_lshl_b64 s[8:9], s[70:71], 12
	s_add_u32 s11, s6, s8
	s_addc_u32 s65, s7, s9
	s_lshl_b32 s8, s64, 7
	s_ashr_i32 s9, s8, 31
	v_mov_b32_e32 v2, v0
	s_lshl_b64 s[8:9], s[8:9], 1
	s_add_u32 s8, s11, s8
	v_readfirstlane_b32 s10, v2
	s_addc_u32 s9, s65, s9
	s_and_b32 s11, s10, 0xc0
	s_add_u32 s8, s8, s11
	s_addc_u32 s9, s9, 0
	v_and_b32_e32 v3, 48, v2
	global_load_dwordx4 v[46:49], v3, s[8:9]
	global_load_dwordx4 v[42:45], v3, s[8:9] offset:2048
	s_ashr_i32 s9, s10, 2
	s_lshl_b32 s8, s66, 8
	s_andn2_b32 s9, s9, 63
	s_add_i32 s9, s9, s8
	v_and_or_b32 v2, v2, 15, s9
	v_lshlrev_b32_e32 v4, 2, v2
	global_load_dword v179, v4, s[14:15] offset:0
	global_load_dword v178, v4, s[14:15] offset:64
	global_load_dword v177, v4, s[14:15] offset:128
	global_load_dword v176, v4, s[14:15] offset:192
	global_load_dword v175, v4, s[14:15] offset:512
	global_load_dword v174, v4, s[14:15] offset:576
	global_load_dword v171, v4, s[14:15] offset:640
	global_load_dword v169, v4, s[14:15] offset:704
	s_andn2_b64 vcc, exec, s[16:17]
	s_cbranch_vccnz .LBB0_3338
	s_barrier
	s_branch .LBB0_3338

.LBB0_3429:
	v_lshlrev_b32_e32 v158, 16, v6
	v_and_b32_e32 v159, 0xffff0000, v6
	v_lshlrev_b32_e32 v154, 16, v8
	v_and_b32_e32 v155, 0xffff0000, v8
	v_lshlrev_b32_e32 v156, 16, v7
	v_and_b32_e32 v157, 0xffff0000, v7
	v_lshlrev_b32_e32 v152, 16, v9
	v_and_b32_e32 v153, 0xffff0000, v9
	s_waitcnt vmcnt(10)
	v_lshlrev_b32_e32 v6, 16, v4
	v_and_b32_e32 v7, 0xffff0000, v4
	v_mul_f32_e32 v4, 0x41000000, v146
	v_pk_fma_f32 v[134:135], v[134:135], s[38:39], v[158:159] op_sel_hi:[1,0,1]
	v_pk_fma_f32 v[130:131], v[130:131], s[38:39], v[154:155] op_sel_hi:[1,0,1]
	v_pk_fma_f32 v[136:137], v[136:137], s[38:39], v[156:157] op_sel_hi:[1,0,1]
	v_pk_mul_f32 v[134:135], v[4:5], v[134:135] op_sel_hi:[0,1]
	v_pk_fma_f32 v[132:133], v[132:133], s[38:39], v[152:153] op_sel_hi:[1,0,1]
	v_pk_mul_f32 v[130:131], v[4:5], v[130:131] op_sel_hi:[0,1]
	v_lshlrev_b32_e32 v150, 16, v2
	v_and_b32_e32 v151, 0xffff0000, v2
	v_lshlrev_b32_e32 v8, 16, v3
	v_and_b32_e32 v9, 0xffff0000, v3
	v_lshlrev_b32_e32 v2, 16, v5
	v_and_b32_e32 v3, 0xffff0000, v5
	v_pk_mul_f32 v[136:137], v[4:5], v[136:137] op_sel_hi:[0,1]
	v_pk_mul_f32 v[132:133], v[4:5], v[132:133] op_sel_hi:[0,1]
	v_med3_f32 v5, v134, s75, v164
	v_med3_f32 v134, v130, s75, v164
	v_med3_f32 v135, v135, s75, v164
	v_cvt_pk_fp8_f32 v130, v5, v135
	v_med3_f32 v136, v136, s75, v164
	v_med3_f32 v5, v137, s75, v164
	v_pk_fma_f32 v[126:127], v[126:127], s[38:39], v[150:151] op_sel_hi:[1,0,1]
	v_pk_fma_f32 v[128:129], v[128:129], s[38:39], v[8:9] op_sel_hi:[1,0,1]
	v_pk_fma_f32 v[122:123], v[122:123], s[38:39], v[6:7] op_sel_hi:[1,0,1]
	v_pk_fma_f32 v[124:125], v[124:125], s[38:39], v[2:3] op_sel_hi:[1,0,1]
	v_cvt_pk_fp8_f32 v130, v136, v5 op_sel:[0,0,1]
	v_pk_mul_f32 v[128:129], v[4:5], v[128:129] op_sel_hi:[0,1]
	v_pk_mul_f32 v[126:127], v[4:5], v[126:127] op_sel_hi:[0,1]
	v_pk_mul_f32 v[124:125], v[4:5], v[124:125] op_sel_hi:[0,1]
	v_pk_mul_f32 v[4:5], v[4:5], v[122:123] op_sel_hi:[0,1]
	v_med3_f32 v146, v131, s75, v164
	v_med3_f32 v122, v126, s75, v164
	v_med3_f32 v123, v4, s75, v164
	v_med3_f32 v126, v127, s75, v164
	v_med3_f32 v127, v5, s75, v164
	v_cvt_pk_fp8_f32 v131, v134, v146
	v_cvt_pk_fp8_f32 v4, v122, v126
	v_cvt_pk_fp8_f32 v5, v123, v127
	v_mov_b32_e32 v171, v0
	v_med3_f32 v132, v132, s75, v164
	v_readfirstlane_b32 s41, v171
	s_lshr_b32 s8, s41, 6
	v_med3_f32 v133, v133, s75, v164
	v_med3_f32 v128, v128, s75, v164
	v_med3_f32 v124, v124, s75, v164
	v_med3_f32 v122, v129, s75, v164
	v_med3_f32 v123, v125, s75, v164
	s_mulk_i32 s8, 0xb00
	v_cvt_pk_fp8_f32 v131, v132, v133 op_sel:[0,0,1]
	v_cvt_pk_fp8_f32 v4, v128, v122 op_sel:[0,0,1]
	v_cvt_pk_fp8_f32 v5, v124, v123 op_sel:[0,0,1]
	s_add_i32 s8, s8, 0
	v_and_b32_e32 v172, 15, v171
	v_lshrrev_b32_e32 v123, 1, v171
	s_add_i32 s43, s8, 0x20000
	v_mul_u32_u24_e32 v122, 0x50, v172
	v_and_b32_e32 v123, 24, v123
	v_add3_u32 v122, s43, v122, v123
	s_and_b32 s9, s41, 0xc0
	ds_write2_b64 v122, v[130:131], v[4:5] offset1:4
	v_bfe_u32 v4, v171, 2, 4
	s_ashr_i32 s41, s41, 2
	v_mul_u32_u24_e32 v5, 0x50, v4
	v_lshlrev_b32_e32 v123, 4, v171
	s_andn2_b32 s41, s41, 63
	v_lshl_or_b32 v4, s50, 8, v4
	v_and_b32_e32 v146, 48, v123
	v_add_u32_e32 v4, s41, v4
	v_mul_f32_e32 v130, 0x41000000, v170
	v_pk_fma_f32 v[118:119], v[118:119], s[38:39], v[158:159] op_sel_hi:[1,0,1]
	v_pk_fma_f32 v[114:115], v[114:115], s[38:39], v[154:155] op_sel_hi:[1,0,1]
	v_add3_u32 v123, s43, v5, v146
	v_ashrrev_i32_e32 v5, 31, v4
	v_pk_mul_f32 v[118:119], v[130:131], v[118:119] op_sel_hi:[0,1]
	v_pk_mul_f32 v[114:115], v[130:131], v[114:115] op_sel_hi:[0,1]
	v_lshl_add_u32 v128, v4, 10, v146
	v_med3_f32 v5, v118, s75, v164
	v_med3_f32 v118, v114, s75, v164
	v_med3_f32 v119, v119, s75, v164
	v_cvt_pk_fp8_f32 v114, v5, v119
	v_pk_fma_f32 v[120:121], v[120:121], s[38:39], v[156:157] op_sel_hi:[1,0,1]
	v_pk_fma_f32 v[116:117], v[116:117], s[38:39], v[152:153] op_sel_hi:[1,0,1]
	v_pk_mul_f32 v[120:121], v[130:131], v[120:121] op_sel_hi:[0,1]
	v_pk_mul_f32 v[116:117], v[130:131], v[116:117] op_sel_hi:[0,1]
	v_med3_f32 v131, v115, s75, v164
	v_pk_fma_f32 v[110:111], v[110:111], s[38:39], v[150:151] op_sel_hi:[1,0,1]
	v_pk_fma_f32 v[106:107], v[106:107], s[38:39], v[6:7] op_sel_hi:[1,0,1]
	v_med3_f32 v120, v120, s75, v164
	v_med3_f32 v5, v121, s75, v164
	v_pk_mul_f32 v[110:111], v[130:131], v[110:111] op_sel_hi:[0,1]
	v_pk_mul_f32 v[106:107], v[130:131], v[106:107] op_sel_hi:[0,1]
	v_cvt_pk_fp8_f32 v114, v120, v5 op_sel:[0,0,1]
	v_med3_f32 v5, v110, s75, v164
	v_med3_f32 v110, v106, s75, v164
	v_med3_f32 v111, v111, s75, v164
	v_cvt_pk_fp8_f32 v106, v5, v111
	v_pk_fma_f32 v[112:113], v[112:113], s[38:39], v[8:9] op_sel_hi:[1,0,1]
	v_pk_mul_f32 v[112:113], v[130:131], v[112:113] op_sel_hi:[0,1]
	v_med3_f32 v112, v112, s75, v164
	v_med3_f32 v5, v113, s75, v164
	v_cvt_pk_fp8_f32 v106, v112, v5 op_sel:[0,0,1]
	v_mul_f32_e32 v112, 0x41000000, v169
	v_pk_fma_f32 v[102:103], v[102:103], s[38:39], v[158:159] op_sel_hi:[1,0,1]
	v_pk_fma_f32 v[98:99], v[98:99], s[38:39], v[154:155] op_sel_hi:[1,0,1]
	v_cvt_pk_fp8_f32 v115, v118, v131
	v_pk_mul_f32 v[102:103], v[112:113], v[102:103] op_sel_hi:[0,1]
	v_pk_mul_f32 v[98:99], v[112:113], v[98:99] op_sel_hi:[0,1]
	v_med3_f32 v5, v102, s75, v164
	v_med3_f32 v102, v98, s75, v164
	v_med3_f32 v103, v103, s75, v164
	v_cvt_pk_fp8_f32 v98, v5, v103
	v_med3_f32 v116, v116, s75, v164
	v_med3_f32 v117, v117, s75, v164
	v_pk_fma_f32 v[104:105], v[104:105], s[38:39], v[156:157] op_sel_hi:[1,0,1]
	v_pk_fma_f32 v[100:101], v[100:101], s[38:39], v[152:153] op_sel_hi:[1,0,1]
	v_cvt_pk_fp8_f32 v115, v116, v117 op_sel:[0,0,1]
	v_med3_f32 v116, v107, s75, v164
	v_pk_mul_f32 v[104:105], v[112:113], v[104:105] op_sel_hi:[0,1]
	v_pk_mul_f32 v[100:101], v[112:113], v[100:101] op_sel_hi:[0,1]
	v_med3_f32 v113, v99, s75, v164
	v_pk_fma_f32 v[94:95], v[94:95], s[38:39], v[150:151] op_sel_hi:[1,0,1]
	v_pk_fma_f32 v[90:91], v[90:91], s[38:39], v[6:7] op_sel_hi:[1,0,1]
	v_cvt_pk_fp8_f32 v107, v110, v116
	v_med3_f32 v104, v104, s75, v164
	v_med3_f32 v5, v105, s75, v164
	v_pk_mul_f32 v[94:95], v[112:113], v[94:95] op_sel_hi:[0,1]
	v_pk_mul_f32 v[90:91], v[112:113], v[90:91] op_sel_hi:[0,1]
	v_pk_fma_f32 v[108:109], v[108:109], s[38:39], v[2:3] op_sel_hi:[1,0,1]
	v_cvt_pk_fp8_f32 v98, v104, v5 op_sel:[0,0,1]
	v_med3_f32 v5, v94, s75, v164
	v_med3_f32 v94, v90, s75, v164
	v_med3_f32 v95, v95, s75, v164
	s_lshl_b32 s8, s62, 8
	ds_read_b128 v[124:127], v123
	v_pk_mul_f32 v[108:109], v[130:131], v[108:109] op_sel_hi:[0,1]
	v_cvt_pk_fp8_f32 v99, v102, v113
	v_cvt_pk_fp8_f32 v90, v5, v95
	s_or_b32 s8, s9, s8
	v_med3_f32 v108, v108, s75, v164
	v_med3_f32 v109, v109, s75, v164
	v_pk_fma_f32 v[96:97], v[96:97], s[38:39], v[8:9] op_sel_hi:[1,0,1]
	s_ashr_i32 s9, s8, 31
	v_cvt_pk_fp8_f32 v107, v108, v109 op_sel:[0,0,1]
	v_pk_mul_f32 v[96:97], v[112:113], v[96:97] op_sel_hi:[0,1]
	s_add_u32 s86, s16, s8
	s_addc_u32 s87, s17, s9
	v_med3_f32 v100, v100, s75, v164
	v_med3_f32 v101, v101, s75, v164
	v_med3_f32 v96, v96, s75, v164
	v_med3_f32 v5, v97, s75, v164
	v_mov_b32_e32 v108, v128
	v_cvt_pk_fp8_f32 v99, v100, v101 op_sel:[0,0,1]
	v_med3_f32 v100, v91, s75, v164
	v_cvt_pk_fp8_f32 v90, v96, v5 op_sel:[0,0,1]
	v_mul_f32_e32 v96, 0x41000000, v168
	v_pk_fma_f32 v[78:79], v[78:79], s[38:39], v[158:159] op_sel_hi:[1,0,1]
	v_pk_fma_f32 v[74:75], v[74:75], s[38:39], v[154:155] op_sel_hi:[1,0,1]
	s_waitcnt lgkmcnt(0)
	global_store_dwordx4 v108, v[124:127], s[86:87]
	v_cvt_pk_fp8_f32 v91, v94, v100
	v_pk_fma_f32 v[80:81], v[80:81], s[38:39], v[156:157] op_sel_hi:[1,0,1]
	v_pk_mul_f32 v[78:79], v[96:97], v[78:79] op_sel_hi:[0,1]
	v_pk_fma_f32 v[76:77], v[76:77], s[38:39], v[152:153] op_sel_hi:[1,0,1]
	v_pk_mul_f32 v[74:75], v[96:97], v[74:75] op_sel_hi:[0,1]
	ds_write2_b64 v122, v[114:115], v[106:107] offset1:4
	v_or_b32_e32 v110, 16, v4
	v_pk_fma_f32 v[92:93], v[92:93], s[38:39], v[2:3] op_sel_hi:[1,0,1]
	v_pk_mul_f32 v[80:81], v[96:97], v[80:81] op_sel_hi:[0,1]
	v_pk_mul_f32 v[76:77], v[96:97], v[76:77] op_sel_hi:[0,1]
	v_med3_f32 v5, v78, s75, v164
	v_med3_f32 v78, v74, s75, v164
	v_med3_f32 v79, v79, s75, v164
	v_med3_f32 v97, v75, s75, v164
	ds_read_b128 v[106:109], v123
	v_ashrrev_i32_e32 v111, 31, v110
	v_pk_mul_f32 v[92:93], v[112:113], v[92:93] op_sel_hi:[0,1]
	v_cvt_pk_fp8_f32 v74, v5, v79
	v_cvt_pk_fp8_f32 v75, v78, v97
	v_lshl_add_u32 v110, v110, 10, v146
	v_med3_f32 v92, v92, s75, v164
	v_med3_f32 v93, v93, s75, v164
	v_cvt_pk_fp8_f32 v91, v92, v93 op_sel:[0,0,1]
	v_pk_fma_f32 v[62:63], v[62:63], s[38:39], v[150:151] op_sel_hi:[1,0,1]
	v_pk_fma_f32 v[58:59], v[58:59], s[38:39], v[6:7] op_sel_hi:[1,0,1]
	s_add_u32 s86, s16, s8
	s_addc_u32 s87, s17, s9
	v_med3_f32 v80, v80, s75, v164
	v_med3_f32 v76, v76, s75, v164
	v_med3_f32 v5, v81, s75, v164
	v_med3_f32 v77, v77, s75, v164
	v_pk_mul_f32 v[62:63], v[96:97], v[62:63] op_sel_hi:[0,1]
	v_pk_mul_f32 v[58:59], v[96:97], v[58:59] op_sel_hi:[0,1]
	v_mov_b32_e32 v92, v110
	v_cvt_pk_fp8_f32 v74, v80, v5 op_sel:[0,0,1]
	v_cvt_pk_fp8_f32 v75, v76, v77 op_sel:[0,0,1]
	v_med3_f32 v5, v62, s75, v164
	v_med3_f32 v62, v58, s75, v164
	v_med3_f32 v63, v63, s75, v164
	v_med3_f32 v76, v59, s75, v164
	s_waitcnt lgkmcnt(0)
	global_store_dwordx4 v92, v[106:109], s[86:87]
	v_cvt_pk_fp8_f32 v58, v5, v63
	v_cvt_pk_fp8_f32 v59, v62, v76
	ds_write2_b64 v122, v[98:99], v[90:91] offset1:4
	v_or_b32_e32 v94, 32, v4
	v_pk_fma_f32 v[64:65], v[64:65], s[38:39], v[8:9] op_sel_hi:[1,0,1]
	v_pk_fma_f32 v[60:61], v[60:61], s[38:39], v[2:3] op_sel_hi:[1,0,1]
	ds_read_b128 v[90:93], v123
	v_ashrrev_i32_e32 v95, 31, v94
	v_pk_mul_f32 v[64:65], v[96:97], v[64:65] op_sel_hi:[0,1]
	v_pk_mul_f32 v[60:61], v[96:97], v[60:61] op_sel_hi:[0,1]
	v_lshl_add_u32 v94, v94, 10, v146
	v_med3_f32 v64, v64, s75, v164
	v_med3_f32 v60, v60, s75, v164
	v_med3_f32 v5, v65, s75, v164
	v_med3_f32 v61, v61, s75, v164
	v_cvt_pk_fp8_f32 v58, v64, v5 op_sel:[0,0,1]
	v_cvt_pk_fp8_f32 v59, v60, v61 op_sel:[0,0,1]
	s_add_u32 s86, s16, s8
	s_addc_u32 s87, s17, s9
	v_mov_b32_e32 v60, v94
	s_waitcnt lgkmcnt(0)
	global_store_dwordx4 v60, v[90:93], s[86:87]
	ds_write2_b64 v122, v[74:75], v[58:59] offset1:4
	v_mul_f32_e32 v64, 0x41000000, v167
	v_pk_fma_f32 v[74:75], v[86:87], s[38:39], v[158:159] op_sel_hi:[1,0,1]
	v_pk_fma_f32 v[78:79], v[82:83], s[38:39], v[154:155] op_sel_hi:[1,0,1]
	v_pk_mul_f32 v[74:75], v[64:65], v[74:75] op_sel_hi:[0,1]
	v_pk_fma_f32 v[76:77], v[88:89], s[38:39], v[156:157] op_sel_hi:[1,0,1]
	v_pk_fma_f32 v[80:81], v[84:85], s[38:39], v[152:153] op_sel_hi:[1,0,1]
	v_pk_mul_f32 v[78:79], v[64:65], v[78:79] op_sel_hi:[0,1]
	v_med3_f32 v5, v74, s75, v164
	v_med3_f32 v75, v75, s75, v164
	v_pk_mul_f32 v[76:77], v[64:65], v[76:77] op_sel_hi:[0,1]
	v_pk_mul_f32 v[80:81], v[64:65], v[80:81] op_sel_hi:[0,1]
	v_med3_f32 v65, v78, s75, v164
	v_med3_f32 v78, v79, s75, v164
	v_cvt_pk_fp8_f32 v74, v5, v75
	v_cvt_pk_fp8_f32 v75, v65, v78
	v_med3_f32 v79, v80, s75, v164
	v_med3_f32 v65, v81, s75, v164
	v_pk_fma_f32 v[70:71], v[70:71], s[38:39], v[150:151] op_sel_hi:[1,0,1]
	v_pk_fma_f32 v[72:73], v[72:73], s[38:39], v[8:9] op_sel_hi:[1,0,1]
	v_pk_fma_f32 v[66:67], v[66:67], s[38:39], v[6:7] op_sel_hi:[1,0,1]
	v_pk_fma_f32 v[68:69], v[68:69], s[38:39], v[2:3] op_sel_hi:[1,0,1]
	v_med3_f32 v76, v76, s75, v164
	v_med3_f32 v5, v77, s75, v164
	v_cvt_pk_fp8_f32 v75, v79, v65 op_sel:[0,0,1]
	v_pk_mul_f32 v[72:73], v[64:65], v[72:73] op_sel_hi:[0,1]
	v_pk_mul_f32 v[70:71], v[64:65], v[70:71] op_sel_hi:[0,1]
	v_pk_mul_f32 v[68:69], v[64:65], v[68:69] op_sel_hi:[0,1]
	v_pk_mul_f32 v[64:65], v[64:65], v[66:67] op_sel_hi:[0,1]
	v_cvt_pk_fp8_f32 v74, v76, v5 op_sel:[0,0,1]
	v_med3_f32 v5, v70, s75, v164
	v_med3_f32 v66, v64, s75, v164
	v_med3_f32 v67, v71, s75, v164
	v_med3_f32 v70, v65, s75, v164
	v_cvt_pk_fp8_f32 v64, v5, v67
	v_cvt_pk_fp8_f32 v65, v66, v70
	v_or_b32_e32 v62, 48, v4
	ds_read_b128 v[58:61], v123
	v_ashrrev_i32_e32 v63, 31, v62
	v_lshl_add_u32 v62, v62, 10, v146
	v_med3_f32 v71, v72, s75, v164
	v_med3_f32 v68, v68, s75, v164
	v_med3_f32 v5, v73, s75, v164
	v_med3_f32 v66, v69, s75, v164
	v_cvt_pk_fp8_f32 v64, v71, v5 op_sel:[0,0,1]
	v_cvt_pk_fp8_f32 v65, v68, v66 op_sel:[0,0,1]
	s_add_u32 s86, s16, s8
	s_addc_u32 s87, s17, s9
	s_waitcnt lgkmcnt(0)
	global_store_dwordx4 v62, v[58:61], s[86:87]
	ds_write2_b64 v122, v[74:75], v[64:65] offset1:4
	v_mul_f32_e32 v64, 0x41000000, v166
	v_pk_fma_f32 v[54:55], v[54:55], s[38:39], v[158:159] op_sel_hi:[1,0,1]
	v_pk_fma_f32 v[50:51], v[50:51], s[38:39], v[154:155] op_sel_hi:[1,0,1]
	v_pk_mul_f32 v[54:55], v[64:65], v[54:55] op_sel_hi:[0,1]
	v_pk_mul_f32 v[50:51], v[64:65], v[50:51] op_sel_hi:[0,1]
	v_med3_f32 v5, v54, s75, v164
	v_med3_f32 v54, v50, s75, v164
	v_med3_f32 v55, v55, s75, v164
	v_cvt_pk_fp8_f32 v50, v5, v55
	v_pk_fma_f32 v[56:57], v[56:57], s[38:39], v[156:157] op_sel_hi:[1,0,1]
	v_pk_fma_f32 v[52:53], v[52:53], s[38:39], v[152:153] op_sel_hi:[1,0,1]
	v_pk_mul_f32 v[56:57], v[64:65], v[56:57] op_sel_hi:[0,1]
	v_pk_mul_f32 v[52:53], v[64:65], v[52:53] op_sel_hi:[0,1]
	v_med3_f32 v65, v51, s75, v164
	v_pk_fma_f32 v[46:47], v[46:47], s[38:39], v[150:151] op_sel_hi:[1,0,1]
	v_pk_fma_f32 v[42:43], v[42:43], s[38:39], v[6:7] op_sel_hi:[1,0,1]
	v_med3_f32 v56, v56, s75, v164
	v_med3_f32 v5, v57, s75, v164
	v_pk_mul_f32 v[46:47], v[64:65], v[46:47] op_sel_hi:[0,1]
	v_pk_mul_f32 v[42:43], v[64:65], v[42:43] op_sel_hi:[0,1]
	v_cvt_pk_fp8_f32 v50, v56, v5 op_sel:[0,0,1]
	v_med3_f32 v5, v46, s75, v164
	v_med3_f32 v46, v42, s75, v164
	v_med3_f32 v47, v47, s75, v164
	v_cvt_pk_fp8_f32 v42, v5, v47
	v_pk_fma_f32 v[48:49], v[48:49], s[38:39], v[8:9] op_sel_hi:[1,0,1]
	v_pk_mul_f32 v[48:49], v[64:65], v[48:49] op_sel_hi:[0,1]
	v_med3_f32 v48, v48, s75, v164
	v_med3_f32 v5, v49, s75, v164
	v_cvt_pk_fp8_f32 v42, v48, v5 op_sel:[0,0,1]
	v_mul_f32_e32 v48, 0x41000000, v165
	v_pk_fma_f32 v[38:39], v[38:39], s[38:39], v[158:159] op_sel_hi:[1,0,1]
	v_pk_fma_f32 v[34:35], v[34:35], s[38:39], v[154:155] op_sel_hi:[1,0,1]
	v_cvt_pk_fp8_f32 v51, v54, v65
	v_pk_mul_f32 v[38:39], v[48:49], v[38:39] op_sel_hi:[0,1]
	v_pk_mul_f32 v[34:35], v[48:49], v[34:35] op_sel_hi:[0,1]
	v_med3_f32 v5, v38, s75, v164
	v_med3_f32 v38, v34, s75, v164
	v_med3_f32 v39, v39, s75, v164
	v_cvt_pk_fp8_f32 v34, v5, v39
	v_med3_f32 v52, v52, s75, v164
	v_med3_f32 v53, v53, s75, v164
	v_pk_fma_f32 v[40:41], v[40:41], s[38:39], v[156:157] op_sel_hi:[1,0,1]
	v_pk_fma_f32 v[36:37], v[36:37], s[38:39], v[152:153] op_sel_hi:[1,0,1]
	v_cvt_pk_fp8_f32 v51, v52, v53 op_sel:[0,0,1]
	v_med3_f32 v52, v43, s75, v164
	v_pk_mul_f32 v[40:41], v[48:49], v[40:41] op_sel_hi:[0,1]
	v_pk_mul_f32 v[36:37], v[48:49], v[36:37] op_sel_hi:[0,1]
	v_med3_f32 v49, v35, s75, v164
	v_pk_fma_f32 v[30:31], v[30:31], s[38:39], v[150:151] op_sel_hi:[1,0,1]
	v_pk_fma_f32 v[26:27], v[26:27], s[38:39], v[6:7] op_sel_hi:[1,0,1]
	v_cvt_pk_fp8_f32 v43, v46, v52
	v_med3_f32 v40, v40, s75, v164
	v_med3_f32 v5, v41, s75, v164
	v_pk_mul_f32 v[30:31], v[48:49], v[30:31] op_sel_hi:[0,1]
	v_pk_mul_f32 v[26:27], v[48:49], v[26:27] op_sel_hi:[0,1]
	v_add_u32_e32 v62, 0x80, v4
	v_pk_fma_f32 v[44:45], v[44:45], s[38:39], v[2:3] op_sel_hi:[1,0,1]
	v_cvt_pk_fp8_f32 v34, v40, v5 op_sel:[0,0,1]
	v_med3_f32 v5, v30, s75, v164
	v_med3_f32 v30, v26, s75, v164
	v_med3_f32 v31, v31, s75, v164
	ds_read_b128 v[58:61], v123
	v_ashrrev_i32_e32 v63, 31, v62
	v_pk_mul_f32 v[44:45], v[64:65], v[44:45] op_sel_hi:[0,1]
	v_cvt_pk_fp8_f32 v35, v38, v49
	v_cvt_pk_fp8_f32 v26, v5, v31
	v_lshl_add_u32 v62, v62, 10, v146
	v_med3_f32 v44, v44, s75, v164
	v_med3_f32 v45, v45, s75, v164
	v_pk_fma_f32 v[32:33], v[32:33], s[38:39], v[8:9] op_sel_hi:[1,0,1]
	v_cvt_pk_fp8_f32 v43, v44, v45 op_sel:[0,0,1]
	v_pk_mul_f32 v[32:33], v[48:49], v[32:33] op_sel_hi:[0,1]
	s_add_u32 s86, s16, s8
	s_addc_u32 s87, s17, s9
	v_med3_f32 v36, v36, s75, v164
	v_med3_f32 v37, v37, s75, v164
	v_med3_f32 v32, v32, s75, v164
	v_med3_f32 v5, v33, s75, v164
	v_mov_b32_e32 v44, v62
	v_cvt_pk_fp8_f32 v35, v36, v37 op_sel:[0,0,1]
	v_med3_f32 v36, v27, s75, v164
	v_cvt_pk_fp8_f32 v26, v32, v5 op_sel:[0,0,1]
	v_mul_f32_e32 v32, 0x41000000, v1
	v_pk_fma_f32 v[22:23], v[22:23], s[38:39], v[158:159] op_sel_hi:[1,0,1]
	v_pk_fma_f32 v[18:19], v[18:19], s[38:39], v[154:155] op_sel_hi:[1,0,1]
	s_waitcnt lgkmcnt(0)
	global_store_dwordx4 v44, v[58:61], s[86:87]
	v_cvt_pk_fp8_f32 v27, v30, v36
	v_pk_mul_f32 v[22:23], v[32:33], v[22:23] op_sel_hi:[0,1]
	v_pk_mul_f32 v[18:19], v[32:33], v[18:19] op_sel_hi:[0,1]
	ds_write2_b64 v122, v[50:51], v[42:43] offset1:4
	v_add_u32_e32 v46, 0x90, v4
	v_pk_fma_f32 v[28:29], v[28:29], s[38:39], v[2:3] op_sel_hi:[1,0,1]
	v_med3_f32 v1, v22, s75, v164
	v_med3_f32 v5, v18, s75, v164
	v_med3_f32 v22, v23, s75, v164
	v_med3_f32 v23, v19, s75, v164
	ds_read_b128 v[42:45], v123
	v_ashrrev_i32_e32 v47, 31, v46
	v_pk_mul_f32 v[28:29], v[48:49], v[28:29] op_sel_hi:[0,1]
	v_cvt_pk_fp8_f32 v18, v1, v22
	v_cvt_pk_fp8_f32 v19, v5, v23
	v_lshl_add_u32 v46, v46, 10, v146
	v_med3_f32 v28, v28, s75, v164
	v_med3_f32 v29, v29, s75, v164
	v_pk_fma_f32 v[24:25], v[24:25], s[38:39], v[156:157] op_sel_hi:[1,0,1]
	v_pk_fma_f32 v[20:21], v[20:21], s[38:39], v[152:153] op_sel_hi:[1,0,1]
	v_cvt_pk_fp8_f32 v27, v28, v29 op_sel:[0,0,1]
	v_pk_mul_f32 v[24:25], v[32:33], v[24:25] op_sel_hi:[0,1]
	v_pk_mul_f32 v[20:21], v[32:33], v[20:21] op_sel_hi:[0,1]
	v_pk_fma_f32 v[14:15], v[14:15], s[38:39], v[150:151] op_sel_hi:[1,0,1]
	v_pk_fma_f32 v[6:7], v[10:11], s[38:39], v[6:7] op_sel_hi:[1,0,1]
	s_add_u32 s86, s16, s8
	s_addc_u32 s87, s17, s9
	v_med3_f32 v24, v24, s75, v164
	v_med3_f32 v20, v20, s75, v164
	v_med3_f32 v1, v25, s75, v164
	v_med3_f32 v5, v21, s75, v164
	v_pk_mul_f32 v[14:15], v[32:33], v[14:15] op_sel_hi:[0,1]
	v_pk_mul_f32 v[6:7], v[32:33], v[6:7] op_sel_hi:[0,1]
	v_mov_b32_e32 v28, v46
	v_cvt_pk_fp8_f32 v18, v24, v1 op_sel:[0,0,1]
	v_cvt_pk_fp8_f32 v19, v20, v5 op_sel:[0,0,1]
	v_med3_f32 v1, v14, s75, v164
	v_med3_f32 v5, v6, s75, v164
	v_med3_f32 v10, v15, s75, v164
	v_med3_f32 v11, v7, s75, v164
	s_waitcnt lgkmcnt(0)
	global_store_dwordx4 v28, v[42:45], s[86:87]
	v_cvt_pk_fp8_f32 v6, v1, v10
	v_cvt_pk_fp8_f32 v7, v5, v11
	ds_write2_b64 v122, v[34:35], v[26:27] offset1:4
	v_add_u32_e32 v30, 0xa0, v4
	v_pk_fma_f32 v[8:9], v[16:17], s[38:39], v[8:9] op_sel_hi:[1,0,1]
	v_pk_fma_f32 v[2:3], v[12:13], s[38:39], v[2:3] op_sel_hi:[1,0,1]
	ds_read_b128 v[26:29], v123
	v_ashrrev_i32_e32 v31, 31, v30
	v_pk_mul_f32 v[8:9], v[32:33], v[8:9] op_sel_hi:[0,1]
	v_pk_mul_f32 v[2:3], v[32:33], v[2:3] op_sel_hi:[0,1]
	v_lshl_add_u32 v30, v30, 10, v146
	v_med3_f32 v8, v8, s75, v164
	v_med3_f32 v2, v2, s75, v164
	v_med3_f32 v1, v9, s75, v164
	v_med3_f32 v3, v3, s75, v164
	v_cvt_pk_fp8_f32 v6, v8, v1 op_sel:[0,0,1]
	v_cvt_pk_fp8_f32 v7, v2, v3 op_sel:[0,0,1]
	s_add_u32 s86, s16, s8
	s_addc_u32 s87, s17, s9
	v_mov_b32_e32 v2, v30
	s_waitcnt lgkmcnt(0)
	global_store_dwordx4 v2, v[26:29], s[86:87]
	ds_write2_b64 v122, v[18:19], v[6:7] offset1:4
	v_add_u32_e32 v2, 0xb0, v4
	ds_read_b128 v[6:9], v123
	v_ashrrev_i32_e32 v3, 31, v2
	v_lshl_add_u32 v2, v2, 10, v146
	s_add_u32 s86, s16, s8
	s_addc_u32 s87, s17, s9
	s_waitcnt lgkmcnt(0)
	global_store_dwordx4 v2, v[6:9], s[86:87]
	s_and_b64 vcc, exec, s[10:11]
	s_mov_b64 s[8:9], -1
	s_cbranch_vccnz .LBB0_3418
	v_mov_b32_e32 v12, v0
	s_lshl_b32 s9, s42, 8
	v_readfirstlane_b32 s8, v12
	s_and_b32 s10, s8, 0xc0
	s_ashr_i32 s8, s8, 2
	s_andn2_b32 s8, s8, 63
	s_add_i32 s8, s8, s9
	v_and_or_b32 v2, v12, 15, s8
	v_lshlrev_b32_e32 v4, 2, v2
	s_lshl_b64 s[8:9], s[44:45], 11
	s_add_u32 s11, s54, s8
	s_addc_u32 s41, s55, s9
	s_lshl_b32 s8, s40, 8
	global_load_dword v146, v4, s[12:13] offset:0
	global_load_dword v170, v4, s[12:13] offset:64
	global_load_dword v169, v4, s[12:13] offset:128
	global_load_dword v168, v4, s[12:13] offset:192
	global_load_dword v167, v4, s[12:13] offset:512
	global_load_dword v166, v4, s[12:13] offset:576
	global_load_dword v165, v4, s[12:13] offset:640
	global_load_dword v1, v4, s[12:13] offset:704
	s_ashr_i32 s9, s8, 31
	s_lshl_b64 s[8:9], s[8:9], 1
	s_add_u32 s8, s11, s8
	s_addc_u32 s9, s41, s9
	s_lshl_b32 s10, s10, 1
	s_add_u32 s8, s8, s10
	s_addc_u32 s9, s9, 0
	v_and_b32_e32 v2, 48, v12
	global_load_dwordx4 v[6:9], v2, s[8:9]
	s_nop 0
	global_load_dwordx4 v[2:5], v2, s[8:9] offset:64
	s_andn2_b64 vcc, exec, s[14:15]
	s_cbranch_vccnz .LBB0_3417
	s_barrier
	s_branch .LBB0_3417
